# running max kept in one register across both halves (no per-iteration copies; rescale blocks update in place; threshold-0 check passed)
# baseline (speedup 1.0000x reference)
; #define PK4(P, BASE, OUT) do { u32x4 w = {cvt_pk_bf16(P[BASE + 0], P[BASE + 1]), cvt_pk_bf16(P[BASE + 2], P[BASE + 3]), cvt_pk_bf16(P[BASE + 4], P[BASE + 5]), cvt_pk_bf16(P[BASE + 6], P[BASE + 7])}; \
;     OUT = *reinterpret_cast<bf16x8*>(&w); } while (0)
; DEVI void finishSM(f32x16& p0, f32x16& p1, float alpha, float& l_reg, bf16x8& pa0, bf16x8& pa1, bf16x8& pa2, bf16x8& pa3) {
; #pragma unroll
;     for (int r = 0; r < 16; ++r) p1[r] = __builtin_amdgcn_exp2f(p1[r]);
;     f32x2 s2 = (f32x2){p0[0], p0[1]} + (f32x2){p1[0], p1[1]};
; #pragma unroll
;     for (int r = 2; r < 16; r += 2) s2 += (f32x2){p0[r], p0[r + 1]} + (f32x2){p1[r], p1[r + 1]};
;     float ps = s2[0] + s2[1];
;     { auto rr = __builtin_amdgcn_permlane32_swap(__float_as_uint(ps), __float_as_uint(ps), false, false);
;       ps = __uint_as_float(rr[0]) + __uint_as_float(rr[1]); }
;     l_reg = l_reg * alpha + ps;
;     ...
;     PK4(p0, 0, pa0); PK4(p0, 8, pa1); PK4(p1, 0, pa2); PK4(p1, 8, pa3);
; DEVI void qkt(f32x16& p0, f32x16& p1, const char* Kb, const bf16x8 (&qr)[6], int r32, int hi, const f32x16& cinit) {
; #pragma unroll
;     for (int d0 = 0; d0 < 6; ++d0) { const int cb = (d0 * 16 + hi * 8) * 2;
;         const bf16x8 k0 = *(const bf16x8*)(Kb + KSWZ(r32, cb)), k1 = *(const bf16x8*)(Kb + KSWZ(32 + r32, cb));
;         p0 = __builtin_amdgcn_mfma_f32_32x32x16_bf16(k0, qr[d0], d0 == 0 ? cinit : p0, 0, 0, 0);
;         p1 = __builtin_amdgcn_mfma_f32_32x32x16_bf16(k1, qr[d0], d0 == 0 ? cinit : p1, 0, 0, 0); }
; }
.LBB0_696:
	v_add_u32_e32 v174, s98, v204
	v_exp_f32_e32 v66, v66
	v_exp_f32_e32 v67, v67
	s_waitcnt lgkmcnt(1)
	v_mfma_f32_32x32x16_bf16 v[98:113], v[82:85], v[150:153], v[34:49]
	v_add_u32_e32 v82, s98, v184
	v_add_u32_e32 v83, s98, v185
	ds_read_b128 v[208:211], v82 offset:12288
	ds_read_b128 v[212:215], v82 offset:18432
	ds_read_b128 v[216:219], v83 offset:12288
	ds_read_b128 v[220:223], v83 offset:18432
	v_exp_f32_e32 v68, v68
	v_exp_f32_e32 v69, v69
	v_exp_f32_e32 v70, v70
	v_exp_f32_e32 v71, v71
	s_waitcnt lgkmcnt(4)
	v_mfma_f32_32x32x16_bf16 v[82:97], v[124:127], v[150:153], v[34:49]
	ds_read_b128 v[124:127], v174 offset:12288
	ds_read_b128 v[224:227], v174 offset:18432
	v_exp_f32_e32 v72, v72
	v_exp_f32_e32 v73, v73
	v_exp_f32_e32 v74, v74
	v_exp_f32_e32 v75, v75
	v_exp_f32_e32 v76, v76
	v_exp_f32_e32 v77, v77
	s_waitcnt lgkmcnt(5)
	v_mfma_f32_32x32x16_bf16 v[98:113], v[208:211], v[138:141], v[98:113]
	v_add_u32_e32 v174, s98, v205
	v_exp_f32_e32 v78, v78
	v_exp_f32_e32 v79, v79
	ds_read_b128 v[228:231], v174 offset:12288
	ds_read_b128 v[232:235], v174 offset:18432
	v_exp_f32_e32 v80, v80
	v_exp_f32_e32 v81, v81
	v_add_u32_e32 v174, s98, v206
	s_waitcnt lgkmcnt(6)
	v_mfma_f32_32x32x16_bf16 v[82:97], v[212:215], v[138:141], v[82:97]
	v_add_f32_e64 v212, v50, v66
	v_add_f32_e64 v213, v51, v67
	v_add_f32_e64 v214, v52, v68
	v_add_f32_e64 v215, v53, v69
	v_lshl_add_u32 v202, s89, 14, v115
	v_add_f32_e32 v212, v214, v212
	v_add_f32_e32 v213, v215, v213
	v_add_f32_e32 v214, v54, v70
	v_add_f32_e32 v215, v55, v71
	ds_read_b128 v[208:211], v174 offset:12288
	ds_read_b128 v[236:239], v174 offset:18432
	v_add_f32_e32 v212, v214, v212
	v_add_f32_e32 v213, v215, v213
	s_waitcnt lgkmcnt(7)
	v_mfma_f32_32x32x16_bf16 v[98:113], v[216:219], v[134:137], v[98:113]
	v_add_f32_e64 v214, v56, v72
	v_add_f32_e64 v215, v57, v73
	v_cvt_pk_bf16_f32 v50, v50, v51
	v_cvt_pk_bf16_f32 v51, v52, v53
	v_cvt_pk_bf16_f32 v52, v54, v55
	v_cvt_pk_bf16_f32 v53, v56, v57
	v_cvt_pk_bf16_f32 v54, v58, v59
	v_add_f32_e64 v212, v214, v212
	v_add_f32_e64 v213, v215, v213
	s_waitcnt lgkmcnt(6)
	v_mfma_f32_32x32x16_bf16 v[82:97], v[220:223], v[134:137], v[82:97]
	v_add_f32_e64 v214, v58, v74
	v_add_f32_e64 v215, v59, v75
	v_cvt_pk_bf16_f32 v55, v60, v61
	v_cvt_pk_bf16_f32 v56, v62, v63
	v_cvt_pk_bf16_f32 v57, v64, v65
	v_cvt_pk_bf16_f32 v58, v66, v67
	v_cvt_pk_bf16_f32 v59, v68, v69
	v_add_f32_e64 v212, v214, v212
	v_add_f32_e64 v213, v215, v213
	s_waitcnt lgkmcnt(5)
	v_mfma_f32_32x32x16_bf16 v[98:113], v[124:127], v[130:133], v[98:113]
	v_add_f32_e64 v214, v60, v76
	v_add_f32_e64 v215, v61, v77
	v_add_f32_e64 v126, v62, v78
	v_add_f32_e64 v127, v63, v79
	v_add_f32_e64 v124, v214, v212
	v_add_f32_e64 v125, v215, v213
	v_cvt_pk_bf16_f32 v60, v70, v71
	v_cvt_pk_bf16_f32 v61, v72, v73
	v_cvt_pk_bf16_f32 v62, v74, v75
	v_cvt_pk_bf16_f32 v63, v76, v77
	s_waitcnt lgkmcnt(4)
	v_mfma_f32_32x32x16_bf16 v[82:97], v[224:227], v[130:133], v[82:97]
	v_add_f32_e64 v124, v126, v124
	v_add_f32_e64 v125, v127, v125
	v_add_f32_e64 v126, v64, v80
	v_add_f32_e64 v127, v65, v81
	v_cvt_pk_bf16_f32 v64, v78, v79
	v_cvt_pk_bf16_f32 v65, v80, v81
	ds_read_b64_tr_b16 v[66:67], v202 offset:0
	ds_read_b64_tr_b16 v[68:69], v202 offset:0x400
	ds_read_b64_tr_b16 v[70:71], v202 offset:0x800
	s_waitcnt lgkmcnt(6)
	v_mfma_f32_32x32x16_bf16 v[98:113], v[228:231], v[146:149], v[98:113]
	ds_read_b64_tr_b16 v[72:73], v202 offset:0xc00
	ds_read_b64_tr_b16 v[74:75], v202 offset:0x1000
	ds_read_b64_tr_b16 v[76:77], v202 offset:0x1400
	ds_read_b64_tr_b16 v[78:79], v202 offset:0x1800
	ds_read_b64_tr_b16 v[80:81], v202 offset:0x1c00
	v_add_f32_e64 v124, v126, v124
	v_add_f32_e64 v125, v127, v125
	s_waitcnt lgkmcnt(10)
	v_mfma_f32_32x32x16_bf16 v[82:97], v[232:235], v[146:149], v[82:97]
	v_add_f32_e32 v124, v124, v125

; DEVI void finishSM(f32x16& p0, f32x16& p1, float alpha, float& l_reg, bf16x8& pa0, bf16x8& pa1, bf16x8& pa2, bf16x8& pa3) {
;     ...
;     float ps = s2[0] + s2[1];
;     { auto rr = __builtin_amdgcn_permlane32_swap(__float_as_uint(ps), __float_as_uint(ps), false, false);
;       ps = __uint_as_float(rr[0]) + __uint_as_float(rr[1]); }
	v_mov_b32_e32 v125, v124


; template <int OFF> DEVI s16x4 tr_read(int vb) { s16x4 r; asm volatile("ds_read_b64_tr_b16 %0, %1 offset:%2" : "=&v"(r) : "v"(vb), "i"(OFF) : "memory"); return r; }
; #define SBAR() __builtin_amdgcn_sched_barrier(0)
; DEVI void pv_both(f32x16& o0, f32x16& o1, int vb, bf16x8 pa0, bf16x8 pa1, bf16x8 pa2, bf16x8 pa3) {
;     const s16x4 a0 = tr_read<v_rd_off(0, 0, 0)>(vb), b0 = tr_read<v_rd_off(0, 0, 1)>(vb), a1 = tr_read<v_rd_off(0, 1, 0)>(vb), b1 = tr_read<v_rd_off(0, 1, 1)>(vb);
;     const s16x4 a2 = tr_read<v_rd_off(0, 2, 0)>(vb), b2 = tr_read<v_rd_off(0, 2, 1)>(vb), a3 = tr_read<v_rd_off(0, 3, 0)>(vb), b3 = tr_read<v_rd_off(0, 3, 1)>(vb);
;     const s16x4 c0 = tr_read<v_rd_off(1, 0, 0)>(vb), d0 = tr_read<v_rd_off(1, 0, 1)>(vb), c1 = tr_read<v_rd_off(1, 1, 0)>(vb), d1 = tr_read<v_rd_off(1, 1, 1)>(vb);
;     const s16x4 c2 = tr_read<v_rd_off(1, 2, 0)>(vb), d2 = tr_read<v_rd_off(1, 2, 1)>(vb), c3 = tr_read<v_rd_off(1, 3, 0)>(vb), d3 = tr_read<v_rd_off(1, 3, 1)>(vb);
;     asm volatile("s_waitcnt lgkmcnt(8)" ::: "memory"); SBAR();
;     ...
;     o0 = __builtin_amdgcn_mfma_f32_32x32x16_bf16(pa0, PK(a0, b0), o0, 0, 0, 0);
;     o0 = __builtin_amdgcn_mfma_f32_32x32x16_bf16(pa1, PK(a1, b1), o0, 0, 0, 0);
;     o0 = __builtin_amdgcn_mfma_f32_32x32x16_bf16(pa2, PK(a2, b2), o0, 0, 0, 0);
;     o0 = __builtin_amdgcn_mfma_f32_32x32x16_bf16(pa3, PK(a3, b3), o0, 0, 0, 0);
;     asm volatile("s_waitcnt lgkmcnt(0)" ::: "memory"); SBAR();
;     o1 = __builtin_amdgcn_mfma_f32_32x32x16_bf16(pa0, PK(c0, d0), o1, 0, 0, 0);
;     o1 = __builtin_amdgcn_mfma_f32_32x32x16_bf16(pa1, PK(c1, d1), o1, 0, 0, 0);
;     o1 = __builtin_amdgcn_mfma_f32_32x32x16_bf16(pa2, PK(c2, d2), o1, 0, 0, 0);
;     o1 = __builtin_amdgcn_mfma_f32_32x32x16_bf16(pa3, PK(c3, d3), o1, 0, 0, 0);
;     ...
; }
; template <bool FIRST> DEVI bool partialSM(f32x16& p0, f32x16& p1, float& m_reg, float& alpha) {
;     float pmax = p0[0];
; #pragma unroll
;     for (int r = 1; r < 16; ++r) pmax = fmaxf(pmax, p0[r]);
; #pragma unroll
;     for (int r = 0; r < 16; ++r) pmax = fmaxf(pmax, p1[r]);
;     { auto rr = __builtin_amdgcn_permlane32_swap(__float_as_uint(pmax), __float_as_uint(pmax), false, false);
;       pmax = fmaxf(__uint_as_float(rr[0]), __uint_as_float(rr[1])); }
	s_waitcnt lgkmcnt(9)
	v_mfma_f32_32x32x16_bf16 v[98:113], v[208:211], v[142:145], v[98:113]
	v_permlane32_swap_b32_e32 v124, v125
	ds_read_b64_tr_b16 v[208:209], v202 offset:0x200
	ds_read_b64_tr_b16 v[210:211], v202 offset:0x600
	ds_read_b64_tr_b16 v[212:213], v202 offset:0xa00
	ds_read_b64_tr_b16 v[214:215], v202 offset:0xe00
	ds_read_b64_tr_b16 v[216:217], v202 offset:0x1200
	ds_read_b64_tr_b16 v[218:219], v202 offset:0x1600
	ds_read_b64_tr_b16 v[220:221], v202 offset:0x1a00
	s_waitcnt lgkmcnt(15)
	v_mfma_f32_32x32x16_bf16 v[82:97], v[236:239], v[142:145], v[82:97]
	ds_read_b64_tr_b16 v[222:223], v202 offset:0x1e00
	s_waitcnt lgkmcnt(14)
	v_mfma_f32_32x32x16_bf16 v[18:33], v[50:53], v[66:69], v[18:33]
	s_waitcnt lgkmcnt(6)
	v_mfma_f32_32x32x16_bf16 v[2:17], v[50:53], v[208:211], v[2:17]
	s_nop 1
	v_max_f32_e32 v249, v99, v99
	v_max_f32_e32 v250, v98, v98
	v_max_f32_e32 v249, v250, v249
	v_max3_f32 v249, v249, v100, v101
	v_max3_f32 v249, v249, v102, v103
	v_max3_f32 v251, v249, v104, v105
	v_max3_f32 v251, v251, v106, v107
	v_exp_f32_e32 v50, v98
	v_exp_f32_e32 v51, v99
	v_exp_f32_e32 v52, v100
	v_exp_f32_e32 v53, v101
	v_mfma_f32_32x32x16_bf16 v[18:33], v[54:57], v[70:73], v[18:33]
	s_waitcnt lgkmcnt(4)
	v_mfma_f32_32x32x16_bf16 v[2:17], v[54:57], v[212:215], v[2:17]
	v_max3_f32 v251, v251, v108, v109
	v_max3_f32 v251, v251, v110, v111
	v_max3_f32 v251, v251, v112, v113
	v_max3_f32 v251, v251, v82, v83
	v_max3_f32 v251, v251, v84, v85
	v_max3_f32 v251, v251, v86, v87
	v_max3_f32 v251, v251, v88, v89
	v_exp_f32_e32 v54, v102
	v_exp_f32_e32 v55, v103
	v_exp_f32_e32 v56, v104
	v_exp_f32_e32 v57, v105
	v_mfma_f32_32x32x16_bf16 v[18:33], v[58:61], v[74:77], v[18:33]
	s_waitcnt lgkmcnt(2)
	v_mfma_f32_32x32x16_bf16 v[2:17], v[58:61], v[216:219], v[2:17]
	v_max3_f32 v251, v251, v90, v91
	v_max3_f32 v251, v251, v92, v93
	v_max3_f32 v251, v251, v94, v95
	v_max3_f32 v251, v251, v96, v97
	v_mov_b32_e32 v252, v251


; template <bool FIRST> DEVI bool partialSM(f32x16& p0, f32x16& p1, float& m_reg, float& alpha) {
;     ...
;     { auto rr = __builtin_amdgcn_permlane32_swap(__float_as_uint(pmax), __float_as_uint(pmax), false, false);
;       pmax = fmaxf(__uint_as_float(rr[0]), __uint_as_float(rr[1])); }
;     if (FIRST) { m_reg = pmax; alpha = 1.f;
; #pragma unroll
;         for (int r = 0; r < 16; ++r) { p0[r] = __builtin_amdgcn_exp2f(p0[r] - pmax); p1[r] = p1[r] - pmax; }
;         return false;
;     } else if (__builtin_expect(__all(pmax <= ATT_THR), 1)) { alpha = 1.f;
; #pragma unroll
;         for (int r = 0; r < 16; ++r) p0[r] = __builtin_amdgcn_exp2f(p0[r]);
;         return false;
	v_exp_f32_e32 v58, v106
	v_exp_f32_e32 v59, v107
	v_permlane32_swap_b32_e32 v251, v252
	v_exp_f32_e32 v60, v108
	v_exp_f32_e32 v61, v109
	v_mfma_f32_32x32x16_bf16 v[18:33], v[62:65], v[78:81], v[18:33]
	s_waitcnt lgkmcnt(0)
	v_mfma_f32_32x32x16_bf16 v[2:17], v[62:65], v[220:223], v[2:17]
	v_exp_f32_e32 v62, v110
	v_exp_f32_e32 v63, v111
	v_exp_f32_e32 v64, v112
	v_exp_f32_e32 v65, v113
	v_max_f32_e32 v252, v252, v252
	v_max_f32_e32 v251, v251, v251
	v_max_f32_e32 v126, v251, v252
	v_cmp_ge_f32_e32 vcc, s79, v126
	s_cmp_lg_u64 vcc, exec
	s_cselect_b64 s[6:7], -1, 0
	s_cbranch_scc1 .LBB0_705
	v_mov_b32_e32 v208, 1.0

; template <bool FIRST> DEVI bool partialSM(f32x16& p0, f32x16& p1, float& m_reg, float& alpha) {
;     ...
;     } else if (__builtin_expect(__all(pmax <= ATT_THR), 1)) { alpha = 1.f;
; #pragma unroll
;         for (int r = 0; r < 16; ++r) p0[r] = __builtin_amdgcn_exp2f(p0[r]);
;         return false;
; DEVI void finishSM(f32x16& p0, f32x16& p1, float alpha, float& l_reg, bf16x8& pa0, bf16x8& pa1, bf16x8& pa2, bf16x8& pa3) {
;     ...
;     for (int r = 0; r < 16; ++r) p1[r] = __builtin_amdgcn_exp2f(p1[r]);
	v_exp_f32_e32 v82, v82
	v_exp_f32_e32 v83, v83
	v_exp_f32_e32 v84, v84
	v_exp_f32_e32 v85, v85
	v_exp_f32_e32 v86, v86
	v_exp_f32_e32 v87, v87
	v_exp_f32_e32 v88, v88
	v_exp_f32_e32 v89, v89
	v_exp_f32_e32 v90, v90
	v_exp_f32_e32 v91, v91
	v_exp_f32_e32 v92, v92
	v_exp_f32_e32 v93, v93
	v_exp_f32_e32 v94, v94
	v_exp_f32_e32 v95, v95
	v_exp_f32_e32 v96, v96
	v_exp_f32_e32 v97, v97
	s_branch .LBB0_699

; DEVI void attn_unit8(const Params& p, char* smem, int unit, int l, int& cvs  , CvRun& crun) {
;     ...
;         const char* Kb = K_lds + s0 * 24576; const int vb = vb0 + s0 * 16384;
;         CvRegs cvr; cv_issue(p, l, cvs, lane, cvr, crun); cvs += (int)gridDim.x * 8;
;         qkt(pB0, pB1, Kb + 12288, qr, r32, hi, cinit);
.LBB0_702:
	s_mul_i32 s98, s2, 0x6000
	s_add_i32 s98, s96, s98
	s_lshl_b32 s99, s2, 14
	s_add_i32 s99, s97, s99
	s_mul_i32 s6, s61, 0x6000
	s_add_i32 s6, s6, 0
	v_add_u32_e32 v249, s6, v129

; DEVI void qkt(f32x16& p0, f32x16& p1, const char* Kb, const bf16x8 (&qr)[6], int r32, int hi, const f32x16& cinit) {
; #pragma unroll
;     for (int d0 = 0; d0 < 6; ++d0) { const int cb = (d0 * 16 + hi * 8) * 2;
;         const bf16x8 k0 = *(const bf16x8*)(Kb + KSWZ(r32, cb)), k1 = *(const bf16x8*)(Kb + KSWZ(32 + r32, cb));
;         p0 = __builtin_amdgcn_mfma_f32_32x32x16_bf16(k0, qr[d0], d0 == 0 ? cinit : p0, 0, 0, 0);
;         p1 = __builtin_amdgcn_mfma_f32_32x32x16_bf16(k1, qr[d0], d0 == 0 ? cinit : p1, 0, 0, 0); }
	s_mov_b32 m0, s98
	s_barrier
	ds_read_b128 v[234:237], v249
	ds_read_b128 v[210:213], v249 offset:6144
	global_load_lds_dwordx4 v118, s[12:13]
	s_waitcnt lgkmcnt(1)
	v_mfma_f32_32x32x16_bf16 v[98:113], v[234:237], v[150:153], v[34:49]
	s_add_i32 m0, s98, 0x2000

; DEVI void qkt(f32x16& p0, f32x16& p1, const char* Kb, const bf16x8 (&qr)[6], int r32, int hi, const f32x16& cinit) {
; #pragma unroll
;     for (int d0 = 0; d0 < 6; ++d0) { const int cb = (d0 * 16 + hi * 8) * 2;
;         const bf16x8 k0 = *(const bf16x8*)(Kb + KSWZ(r32, cb)), k1 = *(const bf16x8*)(Kb + KSWZ(32 + r32, cb));
;         p0 = __builtin_amdgcn_mfma_f32_32x32x16_bf16(k0, qr[d0], d0 == 0 ? cinit : p0, 0, 0, 0);
;         p1 = __builtin_amdgcn_mfma_f32_32x32x16_bf16(k1, qr[d0], d0 == 0 ? cinit : p1, 0, 0, 0); }
	v_add_u32_e32 v126, s6, v184
	global_load_lds_dwordx4 v120, s[12:13]
	s_waitcnt lgkmcnt(0)
	v_mfma_f32_32x32x16_bf16 v[66:81], v[210:213], v[150:153], v[34:49]
	ds_read_b128 v[210:213], v126
	ds_read_b128 v[214:217], v126 offset:6144
	s_add_i32 m0, s98, 0x4000

; DEVI void qkt(f32x16& p0, f32x16& p1, const char* Kb, const bf16x8 (&qr)[6], int r32, int hi, const f32x16& cinit) {
; #pragma unroll
;     for (int d0 = 0; d0 < 6; ++d0) { const int cb = (d0 * 16 + hi * 8) * 2;
;         const bf16x8 k0 = *(const bf16x8*)(Kb + KSWZ(r32, cb)), k1 = *(const bf16x8*)(Kb + KSWZ(32 + r32, cb));
;         p0 = __builtin_amdgcn_mfma_f32_32x32x16_bf16(k0, qr[d0], d0 == 0 ? cinit : p0, 0, 0, 0);
;         p1 = __builtin_amdgcn_mfma_f32_32x32x16_bf16(k1, qr[d0], d0 == 0 ? cinit : p1, 0, 0, 0); }
	v_add_u32_e32 v126, s6, v185
	global_load_lds_dwordx4 v122, s[12:13]
	s_mov_b32 m0, s99
	s_waitcnt lgkmcnt(1)
	v_mfma_f32_32x32x16_bf16 v[98:113], v[210:213], v[138:141], v[98:113]


	global_load_lds_dwordx4 v116, s[44:45]
	s_add_i32 m0, s99, 0x2000


; template <int OFF> DEVI s16x4 tr_read(int vb) { s16x4 r; asm volatile("ds_read_b64_tr_b16 %0, %1 offset:%2" : "=&v"(r) : "v"(vb), "i"(OFF) : "memory"); return r; }
; DEVI void pv_both(f32x16& o0, f32x16& o1, int vb, bf16x8 pa0, bf16x8 pa1, bf16x8 pa2, bf16x8 pa3) {
;     const s16x4 a0 = tr_read<v_rd_off(0, 0, 0)>(vb), b0 = tr_read<v_rd_off(0, 0, 1)>(vb), a1 = tr_read<v_rd_off(0, 1, 0)>(vb), b1 = tr_read<v_rd_off(0, 1, 1)>(vb);
;     const s16x4 a2 = tr_read<v_rd_off(0, 2, 0)>(vb), b2 = tr_read<v_rd_off(0, 2, 1)>(vb), a3 = tr_read<v_rd_off(0, 3, 0)>(vb), b3 = tr_read<v_rd_off(0, 3, 1)>(vb);
;     const s16x4 c0 = tr_read<v_rd_off(1, 0, 0)>(vb), d0 = tr_read<v_rd_off(1, 0, 1)>(vb), c1 = tr_read<v_rd_off(1, 1, 0)>(vb), d1 = tr_read<v_rd_off(1, 1, 1)>(vb);
;     const s16x4 c2 = tr_read<v_rd_off(1, 2, 0)>(vb), d2 = tr_read<v_rd_off(1, 2, 1)>(vb), c3 = tr_read<v_rd_off(1, 3, 0)>(vb), d3 = tr_read<v_rd_off(1, 3, 1)>(vb);
; DEVI void finishSM(f32x16& p0, f32x16& p1, float alpha, float& l_reg, bf16x8& pa0, bf16x8& pa1, bf16x8& pa2, bf16x8& pa3) {
; #pragma unroll
;     for (int r = 0; r < 16; ++r) p1[r] = __builtin_amdgcn_exp2f(p1[r]);
;     f32x2 s2 = (f32x2){p0[0], p0[1]} + (f32x2){p1[0], p1[1]};
; #pragma unroll
;     for (int r = 2; r < 16; r += 2) s2 += (f32x2){p0[r], p0[r + 1]} + (f32x2){p1[r], p1[r + 1]};
;     float ps = s2[0] + s2[1];
;     { auto rr = __builtin_amdgcn_permlane32_swap(__float_as_uint(ps), __float_as_uint(ps), false, false);
;       ps = __uint_as_float(rr[0]) + __uint_as_float(rr[1]); }
;     l_reg = l_reg * alpha + ps;
;     ...
;     PK4(p0, 0, pa0); PK4(p0, 8, pa1); PK4(p1, 0, pa2); PK4(p1, 8, pa3);
;     ...
; }
; DEVI void qkt(f32x16& p0, f32x16& p1, const char* Kb, const bf16x8 (&qr)[6], int r32, int hi, const f32x16& cinit) {
; #pragma unroll
;     for (int d0 = 0; d0 < 6; ++d0) { const int cb = (d0 * 16 + hi * 8) * 2;
;         const bf16x8 k0 = *(const bf16x8*)(Kb + KSWZ(r32, cb)), k1 = *(const bf16x8*)(Kb + KSWZ(32 + r32, cb));
;         p0 = __builtin_amdgcn_mfma_f32_32x32x16_bf16(k0, qr[d0], d0 == 0 ? cinit : p0, 0, 0, 0);
;         p1 = __builtin_amdgcn_mfma_f32_32x32x16_bf16(k1, qr[d0], d0 == 0 ? cinit : p1, 0, 0, 0); }
	s_waitcnt lgkmcnt(0)
	v_mfma_f32_32x32x16_bf16 v[66:81], v[214:217], v[138:141], v[66:81]
	global_load_lds_dwordx4 v117, s[44:45]
	ds_read_b128 v[210:213], v126
	ds_read_b128 v[214:217], v126 offset:6144
	v_add_u32_e32 v126, s6, v204
	s_waitcnt lgkmcnt(1)
	v_mfma_f32_32x32x16_bf16 v[98:113], v[210:213], v[134:137], v[98:113]
	ds_read_b128 v[210:213], v126
	ds_read_b128 v[218:221], v126 offset:6144
	v_add_u32_e32 v126, s6, v205
	s_waitcnt lgkmcnt(2)
	v_mfma_f32_32x32x16_bf16 v[66:81], v[214:217], v[134:137], v[66:81]
	ds_read_b128 v[214:217], v126
	ds_read_b128 v[222:225], v126 offset:6144
	v_add_u32_e32 v126, s6, v206
	ds_read_b128 v[226:229], v126
	ds_read_b128 v[230:233], v126 offset:6144
	v_add_f32_e32 v126, v50, v82
	v_add_f32_e32 v127, v51, v83
	v_cvt_pk_bf16_f32 v50, v50, v51
	v_cvt_pk_bf16_f32 v51, v52, v53
	s_waitcnt lgkmcnt(5)
	v_mfma_f32_32x32x16_bf16 v[98:113], v[210:213], v[130:133], v[98:113]
	v_add_f32_e64 v210, v52, v84
	v_add_f32_e64 v211, v53, v85
	v_cvt_pk_bf16_f32 v52, v54, v55
	v_cvt_pk_bf16_f32 v53, v56, v57
	v_add_f32_e64 v126, v210, v126
	v_add_f32_e64 v127, v211, v127
	v_add_f32_e64 v210, v54, v86
	v_add_f32_e64 v211, v55, v87
	v_cvt_pk_bf16_f32 v54, v58, v59
	s_waitcnt lgkmcnt(4)
	v_mfma_f32_32x32x16_bf16 v[66:81], v[218:221], v[130:133], v[66:81]
	v_add_f32_e64 v126, v210, v126
	v_add_f32_e64 v127, v211, v127
	v_add_f32_e64 v210, v56, v88
	v_add_f32_e64 v211, v57, v89
	v_cvt_pk_bf16_f32 v55, v60, v61
	v_cvt_pk_bf16_f32 v56, v62, v63
	v_cvt_pk_bf16_f32 v57, v64, v65
	v_add_f32_e64 v126, v210, v126
	v_add_f32_e64 v127, v211, v127
	v_add_f32_e32 v210, v58, v90
	v_add_f32_e32 v211, v59, v91
	v_cvt_pk_bf16_f32 v58, v82, v83
	v_cvt_pk_bf16_f32 v59, v84, v85
	s_waitcnt lgkmcnt(3)
	v_mfma_f32_32x32x16_bf16 v[98:113], v[214:217], v[146:149], v[98:113]
	v_add_f32_e64 v126, v210, v126
	v_add_f32_e64 v127, v211, v127
	v_add_f32_e64 v210, v60, v92
	v_add_f32_e64 v211, v61, v93
	v_cvt_pk_bf16_f32 v60, v86, v87
	v_cvt_pk_bf16_f32 v61, v88, v89
	v_add_f32_e64 v126, v210, v126
	v_add_f32_e64 v127, v211, v127
	v_add_f32_e32 v210, v62, v94
	v_add_f32_e32 v211, v63, v95
	v_cvt_pk_bf16_f32 v62, v90, v91
	v_cvt_pk_bf16_f32 v63, v92, v93
	s_waitcnt lgkmcnt(2)
	v_mfma_f32_32x32x16_bf16 v[66:81], v[222:225], v[146:149], v[66:81]
	v_add_f32_e64 v126, v210, v126
	v_add_f32_e64 v127, v211, v127
	v_add_f32_e64 v210, v64, v96
	v_add_f32_e64 v211, v65, v97
	v_cvt_pk_bf16_f32 v64, v94, v95
	v_cvt_pk_bf16_f32 v65, v96, v97
	ds_read_b64_tr_b16 v[154:155], v202 offset:0x2000
	ds_read_b64_tr_b16 v[156:157], v202 offset:0x2400
	ds_read_b64_tr_b16 v[158:159], v202 offset:0x2800
	ds_read_b64_tr_b16 v[160:161], v202 offset:0x2c00
	ds_read_b64_tr_b16 v[162:163], v202 offset:0x3000
	ds_read_b64_tr_b16 v[164:165], v202 offset:0x3400
	ds_read_b64_tr_b16 v[166:167], v202 offset:0x3800
	ds_read_b64_tr_b16 v[168:169], v202 offset:0x3c00
	v_add_f32_e64 v126, v210, v126
	v_add_f32_e64 v127, v211, v127
	ds_read_b64_tr_b16 v[210:211], v202 offset:0x2200
	ds_read_b64_tr_b16 v[212:213], v202 offset:0x2600
	ds_read_b64_tr_b16 v[214:215], v202 offset:0x2a00
	s_waitcnt lgkmcnt(12)
	v_mfma_f32_32x32x16_bf16 v[98:113], v[226:229], v[142:145], v[98:113]
	ds_read_b64_tr_b16 v[216:217], v202 offset:0x2e00
	ds_read_b64_tr_b16 v[218:219], v202 offset:0x3200
	ds_read_b64_tr_b16 v[220:221], v202 offset:0x3600
	ds_read_b64_tr_b16 v[222:223], v202 offset:0x3a00
	ds_read_b64_tr_b16 v[224:225], v202 offset:0x3e00
	v_add_f32_e32 v126, v126, v127
	s_waitcnt lgkmcnt(15)
	v_mfma_f32_32x32x16_bf16 v[66:81], v[230:233], v[142:145], v[66:81]
	v_mov_b32_e32 v127, v126


; #define SBAR() __builtin_amdgcn_sched_barrier(0)
; DEVI void pv_both(f32x16& o0, f32x16& o1, int vb, bf16x8 pa0, bf16x8 pa1, bf16x8 pa2, bf16x8 pa3) {
;     ...
;     o0 = __builtin_amdgcn_mfma_f32_32x32x16_bf16(pa0, PK(a0, b0), o0, 0, 0, 0);
;     o0 = __builtin_amdgcn_mfma_f32_32x32x16_bf16(pa1, PK(a1, b1), o0, 0, 0, 0);
;     o0 = __builtin_amdgcn_mfma_f32_32x32x16_bf16(pa2, PK(a2, b2), o0, 0, 0, 0);
;     o0 = __builtin_amdgcn_mfma_f32_32x32x16_bf16(pa3, PK(a3, b3), o0, 0, 0, 0);
;     asm volatile("s_waitcnt lgkmcnt(0)" ::: "memory"); SBAR();
;     o1 = __builtin_amdgcn_mfma_f32_32x32x16_bf16(pa0, PK(c0, d0), o1, 0, 0, 0);
;     o1 = __builtin_amdgcn_mfma_f32_32x32x16_bf16(pa1, PK(c1, d1), o1, 0, 0, 0);
;     o1 = __builtin_amdgcn_mfma_f32_32x32x16_bf16(pa2, PK(c2, d2), o1, 0, 0, 0);
;     o1 = __builtin_amdgcn_mfma_f32_32x32x16_bf16(pa3, PK(c3, d3), o1, 0, 0, 0);
;     ...
; }
; template <bool FIRST> DEVI bool partialSM(f32x16& p0, f32x16& p1, float& m_reg, float& alpha) {
;     float pmax = p0[0];
; #pragma unroll
;     for (int r = 1; r < 16; ++r) pmax = fmaxf(pmax, p0[r]);
; #pragma unroll
;     for (int r = 0; r < 16; ++r) pmax = fmaxf(pmax, p1[r]);
;     { auto rr = __builtin_amdgcn_permlane32_swap(__float_as_uint(pmax), __float_as_uint(pmax), false, false);
;       pmax = fmaxf(__uint_as_float(rr[0]), __uint_as_float(rr[1])); }
;     if (FIRST) { m_reg = pmax; alpha = 1.f;
; #pragma unroll
;         for (int r = 0; r < 16; ++r) { p0[r] = __builtin_amdgcn_exp2f(p0[r] - pmax); p1[r] = p1[r] - pmax; }
;         return false;
;     } else if (__builtin_expect(__all(pmax <= ATT_THR), 1)) { alpha = 1.f;
; #pragma unroll
;         for (int r = 0; r < 16; ++r) p0[r] = __builtin_amdgcn_exp2f(p0[r]);
	s_waitcnt lgkmcnt(14)
	v_mfma_f32_32x32x16_bf16 v[18:33], v[50:53], v[154:157], v[18:33]
	v_permlane32_swap_b32_e32 v126, v127
	s_waitcnt lgkmcnt(6)
	v_mfma_f32_32x32x16_bf16 v[2:17], v[50:53], v[210:213], v[2:17]
	s_nop 1
	v_max_f32_e32 v249, v99, v99
	v_max_f32_e32 v250, v98, v98
	v_max_f32_e32 v249, v250, v249
	v_max3_f32 v249, v249, v100, v101
	v_max3_f32 v249, v249, v102, v103
	v_max3_f32 v251, v249, v104, v105
	v_max3_f32 v251, v251, v106, v107
	v_exp_f32_e32 v50, v98
	v_exp_f32_e32 v51, v99
	v_exp_f32_e32 v52, v100
	v_exp_f32_e32 v53, v101
	v_mfma_f32_32x32x16_bf16 v[18:33], v[54:57], v[158:161], v[18:33]
	s_waitcnt lgkmcnt(4)
	v_mfma_f32_32x32x16_bf16 v[2:17], v[54:57], v[214:217], v[2:17]
	v_max3_f32 v251, v251, v108, v109
	v_max3_f32 v251, v251, v110, v111
	v_max3_f32 v251, v251, v112, v113
	v_max3_f32 v251, v251, v66, v67
	v_max3_f32 v251, v251, v68, v69
	v_max3_f32 v251, v251, v70, v71
	v_max3_f32 v251, v251, v72, v73
	v_exp_f32_e32 v54, v102
	v_exp_f32_e32 v55, v103
	v_exp_f32_e32 v56, v104
	v_exp_f32_e32 v57, v105
	v_mfma_f32_32x32x16_bf16 v[18:33], v[58:61], v[162:165], v[18:33]
	s_waitcnt lgkmcnt(2)
	v_mfma_f32_32x32x16_bf16 v[2:17], v[58:61], v[218:221], v[2:17]
	v_max3_f32 v251, v251, v74, v75
	v_max3_f32 v251, v251, v76, v77
	v_max3_f32 v251, v251, v78, v79
	v_max3_f32 v251, v251, v80, v81
	v_mov_b32_e32 v252, v251


; DEVI void pv_both(f32x16& o0, f32x16& o1, int vb, bf16x8 pa0, bf16x8 pa1, bf16x8 pa2, bf16x8 pa3) {
;     ...
;     o1 = __builtin_amdgcn_mfma_f32_32x32x16_bf16(pa1, PK(c1, d1), o1, 0, 0, 0);
;     o1 = __builtin_amdgcn_mfma_f32_32x32x16_bf16(pa2, PK(c2, d2), o1, 0, 0, 0);
;     o1 = __builtin_amdgcn_mfma_f32_32x32x16_bf16(pa3, PK(c3, d3), o1, 0, 0, 0);
;     ...
; }
; template <bool FIRST> DEVI bool partialSM(f32x16& p0, f32x16& p1, float& m_reg, float& alpha) {
;     float pmax = p0[0];
; #pragma unroll
;     for (int r = 1; r < 16; ++r) pmax = fmaxf(pmax, p0[r]);
; #pragma unroll
;     for (int r = 0; r < 16; ++r) pmax = fmaxf(pmax, p1[r]);
;     { auto rr = __builtin_amdgcn_permlane32_swap(__float_as_uint(pmax), __float_as_uint(pmax), false, false);
;       pmax = fmaxf(__uint_as_float(rr[0]), __uint_as_float(rr[1])); }
;     if (FIRST) { m_reg = pmax; alpha = 1.f;
; #pragma unroll
;         for (int r = 0; r < 16; ++r) { p0[r] = __builtin_amdgcn_exp2f(p0[r] - pmax); p1[r] = p1[r] - pmax; }
;         return false;
;     } else if (__builtin_expect(__all(pmax <= ATT_THR), 1)) { alpha = 1.f;
; #pragma unroll
;         for (int r = 0; r < 16; ++r) p0[r] = __builtin_amdgcn_exp2f(p0[r]);
;         return false;
;     } else { const float d = fmaxf(pmax, 0.f); alpha = __builtin_amdgcn_exp2f(-d); m_reg += d;
	v_exp_f32_e32 v58, v106
	v_exp_f32_e32 v59, v107
	v_permlane32_swap_b32_e32 v251, v252
	v_exp_f32_e32 v60, v108
	v_exp_f32_e32 v61, v109
	v_mfma_f32_32x32x16_bf16 v[18:33], v[62:65], v[166:169], v[18:33]
	s_waitcnt lgkmcnt(0)
	v_mfma_f32_32x32x16_bf16 v[2:17], v[62:65], v[222:225], v[2:17]
	v_exp_f32_e32 v62, v110
	v_exp_f32_e32 v63, v111
	v_exp_f32_e32 v64, v112
	v_exp_f32_e32 v65, v113
	v_max_f32_e32 v252, v252, v252
	v_max_f32_e32 v251, v251, v251
	v_max_f32_e32 v174, v251, v252
	v_cmp_ge_f32_e32 vcc, s79, v174
	s_cmp_lg_u64 vcc, exec
	s_cselect_b64 s[6:7], -1, 0
	s_cbranch_scc1 .LBB0_711
	v_mov_b32_e32 v202, 1.0

; template <bool FIRST> DEVI bool partialSM(f32x16& p0, f32x16& p1, float& m_reg, float& alpha) {
;     ...
;     } else if (__builtin_expect(__all(pmax <= ATT_THR), 1)) { alpha = 1.f;
; #pragma unroll
;         for (int r = 0; r < 16; ++r) p0[r] = __builtin_amdgcn_exp2f(p0[r]);
;         return false;
	s_branch .LBB0_716

; #define LAS __attribute__((address_space(3)))
; DEVI int v_rd_base(int lane) { return ((lane & 3) << 3) | (((lane >> 2) & 3) << 6) | (((lane >> 4) & 1) << 5) | (((lane >> 5) & 1) << 8); }
; #define VM0() asm volatile("s_waitcnt vmcnt(0)" ::: "memory")
; template <bool FIRST> DEVI bool partialSM(f32x16& p0, f32x16& p1, float& m_reg, float& alpha) {
;     ...
;     } else { const float d = fmaxf(pmax, 0.f); alpha = __builtin_amdgcn_exp2f(-d); m_reg += d;
; #pragma unroll
;         for (int r = 0; r < 16; ++r) { p0[r] = __builtin_amdgcn_exp2f(p0[r] - d); p1[r] = p1[r] - d; }
;         return true;
; DEVI void attn_unit8(const Params& p, char* smem, int unit, int l, int& cvs  , CvRun& crun) {
;     ...
;     const int vb0 = (int)(uintptr_t)(LAS char*)V_lds + v_rd_base(lane);
;     float m_reg = 0.f, l_reg = 0.f; f32x16 o[2];
; #pragma unroll
;     for (int d = 0; d < 2; ++d)
; #pragma unroll
;         for (int r = 0; r < 16; ++r) o[d][r] = 0.f;
;     f32x16 pA0, pA1, pB0, pB1; float alA, alB; bf16x8 pa0, pa1, pa2, pa3;
;     constexpr int NTILE = S_ / 128;
;     B_DMA(0, 0); B_DMA(1, 1); VM0(); __syncthreads();
;     f32x16 cinit;
.LBB0_705:
	v_max_f32_e32 v50, v126, v126
	v_max_f32_e32 v66, 0, v50
	v_sub_f32_e32 v50, v98, v66
	v_sub_f32_e32 v51, v99, v66
	v_sub_f32_e32 v52, v100, v66
	v_sub_f32_e32 v53, v101, v66
	v_sub_f32_e32 v54, v102, v66
	v_sub_f32_e32 v55, v103, v66
	v_sub_f32_e32 v56, v104, v66
	v_sub_f32_e32 v57, v105, v66
	v_sub_f32_e32 v58, v106, v66
	v_sub_f32_e32 v59, v107, v66
	v_sub_f32_e32 v60, v108, v66
	v_sub_f32_e32 v61, v109, v66
	v_sub_f32_e32 v62, v110, v66
	v_sub_f32_e32 v63, v111, v66
	v_sub_f32_e32 v64, v112, v66
	v_sub_f32_e32 v65, v113, v66
	v_exp_f32_e64 v208, -v66
	v_add_f32_e32 v203, v203, v66
	v_exp_f32_e32 v50, v50
	v_exp_f32_e32 v51, v51
	v_exp_f32_e32 v52, v52
	v_exp_f32_e32 v53, v53
	v_exp_f32_e32 v54, v54
	v_exp_f32_e32 v55, v55
	v_exp_f32_e32 v56, v56
	v_exp_f32_e32 v57, v57
	v_exp_f32_e32 v58, v58
	v_exp_f32_e32 v59, v59
	v_exp_f32_e32 v60, v60
	v_exp_f32_e32 v61, v61
	v_exp_f32_e32 v62, v62
	v_exp_f32_e32 v63, v63
	v_exp_f32_e32 v64, v64
	v_exp_f32_e32 v65, v65
	v_sub_f32_e32 v97, v97, v66
	v_sub_f32_e32 v96, v96, v66
	v_sub_f32_e32 v95, v95, v66
	v_sub_f32_e32 v94, v94, v66
	v_sub_f32_e32 v93, v93, v66
	v_sub_f32_e32 v92, v92, v66
	v_sub_f32_e32 v91, v91, v66
	v_sub_f32_e32 v90, v90, v66
	v_sub_f32_e32 v89, v89, v66
	v_sub_f32_e32 v88, v88, v66
	v_sub_f32_e32 v87, v87, v66
	v_sub_f32_e32 v86, v86, v66
	v_sub_f32_e32 v85, v85, v66
	v_sub_f32_e32 v84, v84, v66
	v_sub_f32_e32 v83, v83, v66
	v_sub_f32_e32 v82, v82, v66
	v_exp_f32_e32 v82, v82
	v_exp_f32_e32 v83, v83
	v_exp_f32_e32 v84, v84
	v_exp_f32_e32 v85, v85
	v_exp_f32_e32 v86, v86
	v_exp_f32_e32 v87, v87
	v_exp_f32_e32 v88, v88
	v_exp_f32_e32 v89, v89
	v_exp_f32_e32 v90, v90
	v_exp_f32_e32 v91, v91
	v_exp_f32_e32 v92, v92
	v_exp_f32_e32 v93, v93
	v_exp_f32_e32 v94, v94
	v_exp_f32_e32 v95, v95
	v_exp_f32_e32 v96, v96
	v_exp_f32_e32 v97, v97
	s_cbranch_execnz .LBB0_698
.LBB0_707:
	s_and_saveexec_b64 s[6:7], s[4:5]
	ds_write_b32 v187, v208 offset:128
	s_or_b64 exec, exec, s[6:7]
	v_add_u32_e32 v46, s91, v178
	s_waitcnt lgkmcnt(0)
	ds_read_b128 v[34:37], v46 offset:224
	ds_read_b128 v[38:41], v46 offset:192
	ds_read_b128 v[42:45], v46 offset:160
	ds_read_b128 v[46:49], v46 offset:128
	s_waitcnt lgkmcnt(0)
	v_pk_mul_f32 v[30:31], v[30:31], v[34:35]
	v_pk_mul_f32 v[14:15], v[14:15], v[34:35]
	v_xor_b32_e32 v34, 0x80000000, v203
	s_waitcnt lgkmcnt(2)
	v_pk_mul_f32 v[26:27], v[26:27], v[38:39]
	s_waitcnt lgkmcnt(1)
	v_pk_mul_f32 v[22:23], v[22:23], v[42:43]
	v_pk_mul_f32 v[32:33], v[32:33], v[36:37]
	v_pk_mul_f32 v[28:29], v[28:29], v[40:41]
	v_pk_mul_f32 v[24:25], v[24:25], v[44:45]
	s_waitcnt lgkmcnt(0)
	v_pk_mul_f32 v[20:21], v[20:21], v[48:49]
	v_pk_mul_f32 v[18:19], v[18:19], v[46:47]
	v_pk_mul_f32 v[10:11], v[10:11], v[38:39]
	v_pk_mul_f32 v[6:7], v[6:7], v[42:43]
	v_pk_mul_f32 v[16:17], v[16:17], v[36:37]
	v_pk_mul_f32 v[12:13], v[12:13], v[40:41]
	v_pk_mul_f32 v[8:9], v[8:9], v[44:45]
	v_pk_mul_f32 v[4:5], v[4:5], v[48:49]
	v_pk_mul_f32 v[2:3], v[2:3], v[46:47]
	v_mov_b32_e32 v35, v34
	v_mov_b32_e32 v36, v34
	v_mov_b32_e32 v37, v34
	v_mov_b32_e32 v38, v34
	v_mov_b32_e32 v39, v34
	v_mov_b32_e32 v40, v34
	v_mov_b32_e32 v41, v34
	v_mov_b32_e32 v42, v34
	v_mov_b32_e32 v43, v34
	v_mov_b32_e32 v44, v34
	v_mov_b32_e32 v45, v34
	v_mov_b32_e32 v46, v34
	v_mov_b32_e32 v47, v34
	v_mov_b32_e32 v48, v34
	v_mov_b32_e32 v49, v34
	s_andn2_b64 vcc, exec, s[14:15]
	s_mov_b64 s[6:7], -1
	s_cbranch_vccnz .LBB0_700

; template <bool FIRST> DEVI bool partialSM(f32x16& p0, f32x16& p1, float& m_reg, float& alpha) {
;     ...
;     } else { const float d = fmaxf(pmax, 0.f); alpha = __builtin_amdgcn_exp2f(-d); m_reg += d;
; #pragma unroll
;         for (int r = 0; r < 16; ++r) { p0[r] = __builtin_amdgcn_exp2f(p0[r] - d); p1[r] = p1[r] - d; }
;         return true;
.LBB0_711:
	v_max_f32_e32 v50, v174, v174
	v_max_f32_e32 v249, 0, v50
	v_sub_f32_e32 v50, v98, v249
	v_sub_f32_e32 v51, v99, v249
	v_sub_f32_e32 v52, v100, v249
	v_sub_f32_e32 v53, v101, v249
	v_sub_f32_e32 v54, v102, v249
	v_sub_f32_e32 v55, v103, v249
	v_sub_f32_e32 v56, v104, v249
	v_sub_f32_e32 v57, v105, v249
	v_sub_f32_e32 v58, v106, v249
	v_sub_f32_e32 v59, v107, v249
	v_sub_f32_e32 v60, v108, v249
	v_sub_f32_e32 v61, v109, v249
	v_sub_f32_e32 v62, v110, v249
	v_sub_f32_e32 v63, v111, v249
	v_sub_f32_e32 v64, v112, v249
	v_sub_f32_e32 v65, v113, v249
	v_exp_f32_e64 v202, -v249
	v_add_f32_e32 v203, v203, v249
	v_exp_f32_e32 v50, v50
	v_exp_f32_e32 v51, v51
	v_exp_f32_e32 v52, v52
	v_exp_f32_e32 v53, v53
	v_exp_f32_e32 v54, v54
	v_exp_f32_e32 v55, v55
	v_exp_f32_e32 v56, v56
	v_exp_f32_e32 v57, v57
	v_exp_f32_e32 v58, v58
	v_exp_f32_e32 v59, v59
	v_exp_f32_e32 v60, v60
	v_exp_f32_e32 v61, v61
	v_exp_f32_e32 v62, v62
	v_exp_f32_e32 v63, v63
	v_exp_f32_e32 v64, v64
	v_exp_f32_e32 v65, v65
	v_sub_f32_e32 v81, v81, v249
	v_sub_f32_e32 v80, v80, v249
	v_sub_f32_e32 v79, v79, v249
	v_sub_f32_e32 v78, v78, v249
	v_sub_f32_e32 v77, v77, v249
	v_sub_f32_e32 v76, v76, v249
	v_sub_f32_e32 v75, v75, v249
	v_sub_f32_e32 v74, v74, v249
	v_sub_f32_e32 v73, v73, v249
	v_sub_f32_e32 v72, v72, v249
	v_sub_f32_e32 v71, v71, v249
	v_sub_f32_e32 v70, v70, v249
	v_sub_f32_e32 v69, v69, v249
	v_sub_f32_e32 v68, v68, v249
	v_sub_f32_e32 v67, v67, v249
	v_sub_f32_e32 v66, v66, v249
	s_cbranch_execnz .LBB0_704

; template <int OFF> DEVI s16x4 tr_read(int vb) { s16x4 r; asm volatile("ds_read_b64_tr_b16 %0, %1 offset:%2" : "=&v"(r) : "v"(vb), "i"(OFF) : "memory"); return r; }
; DEVI void pv_both(f32x16& o0, f32x16& o1, int vb, bf16x8 pa0, bf16x8 pa1, bf16x8 pa2, bf16x8 pa3) {
;     const s16x4 a0 = tr_read<v_rd_off(0, 0, 0)>(vb), b0 = tr_read<v_rd_off(0, 0, 1)>(vb), a1 = tr_read<v_rd_off(0, 1, 0)>(vb), b1 = tr_read<v_rd_off(0, 1, 1)>(vb);
;     const s16x4 a2 = tr_read<v_rd_off(0, 2, 0)>(vb), b2 = tr_read<v_rd_off(0, 2, 1)>(vb), a3 = tr_read<v_rd_off(0, 3, 0)>(vb), b3 = tr_read<v_rd_off(0, 3, 1)>(vb);
;     const s16x4 c0 = tr_read<v_rd_off(1, 0, 0)>(vb), d0 = tr_read<v_rd_off(1, 0, 1)>(vb), c1 = tr_read<v_rd_off(1, 1, 0)>(vb), d1 = tr_read<v_rd_off(1, 1, 1)>(vb);
;     const s16x4 c2 = tr_read<v_rd_off(1, 2, 0)>(vb), d2 = tr_read<v_rd_off(1, 2, 1)>(vb), c3 = tr_read<v_rd_off(1, 3, 0)>(vb), d3 = tr_read<v_rd_off(1, 3, 1)>(vb);
; DEVI void finishSM(f32x16& p0, f32x16& p1, float alpha, float& l_reg, bf16x8& pa0, bf16x8& pa1, bf16x8& pa2, bf16x8& pa3) {
; #pragma unroll
;     for (int r = 0; r < 16; ++r) p1[r] = __builtin_amdgcn_exp2f(p1[r]);
;     f32x2 s2 = (f32x2){p0[0], p0[1]} + (f32x2){p1[0], p1[1]};
; #pragma unroll
;     for (int r = 2; r < 16; r += 2) s2 += (f32x2){p0[r], p0[r + 1]} + (f32x2){p1[r], p1[r + 1]};
;     float ps = s2[0] + s2[1];
;     { auto rr = __builtin_amdgcn_permlane32_swap(__float_as_uint(ps), __float_as_uint(ps), false, false);
;       ps = __uint_as_float(rr[0]) + __uint_as_float(rr[1]); }
;     l_reg = l_reg * alpha + ps;
;     ...
;     PK4(p0, 0, pa0); PK4(p0, 8, pa1); PK4(p1, 0, pa2); PK4(p1, 8, pa3);
;     ...
; }
; DEVI void qkt(f32x16& p0, f32x16& p1, const char* Kb, const bf16x8 (&qr)[6], int r32, int hi, const f32x16& cinit) {
; #pragma unroll
;     for (int d0 = 0; d0 < 6; ++d0) { const int cb = (d0 * 16 + hi * 8) * 2;
;         const bf16x8 k0 = *(const bf16x8*)(Kb + KSWZ(r32, cb)), k1 = *(const bf16x8*)(Kb + KSWZ(32 + r32, cb));
;         p0 = __builtin_amdgcn_mfma_f32_32x32x16_bf16(k0, qr[d0], d0 == 0 ? cinit : p0, 0, 0, 0);
;         p1 = __builtin_amdgcn_mfma_f32_32x32x16_bf16(k1, qr[d0], d0 == 0 ? cinit : p1, 0, 0, 0); }
.LBB0_2260:
	v_add_u32_e32 v174, s98, v205
	v_exp_f32_e32 v66, v66
	v_exp_f32_e32 v67, v67
	s_waitcnt lgkmcnt(1)
	v_mfma_f32_32x32x16_bf16 v[98:113], v[82:85], v[150:153], v[34:49]
	v_add_u32_e32 v82, s98, v184
	v_add_u32_e32 v83, s98, v185
	ds_read_b128 v[210:213], v82 offset:12288
	ds_read_b128 v[214:217], v82 offset:18432
	ds_read_b128 v[218:221], v83 offset:12288
	ds_read_b128 v[222:225], v83 offset:18432
	v_exp_f32_e32 v68, v68
	v_exp_f32_e32 v69, v69
	v_exp_f32_e32 v70, v70
	v_exp_f32_e32 v71, v71
	s_waitcnt lgkmcnt(4)
	v_mfma_f32_32x32x16_bf16 v[82:97], v[124:127], v[150:153], v[34:49]
	ds_read_b128 v[124:127], v174 offset:12288
	ds_read_b128 v[226:229], v174 offset:18432
	v_exp_f32_e32 v72, v72
	v_exp_f32_e32 v73, v73
	v_exp_f32_e32 v74, v74
	v_exp_f32_e32 v75, v75
	v_exp_f32_e32 v76, v76
	v_exp_f32_e32 v77, v77
	s_waitcnt lgkmcnt(5)
	v_mfma_f32_32x32x16_bf16 v[98:113], v[210:213], v[138:141], v[98:113]
	v_add_u32_e32 v174, s98, v206
	v_exp_f32_e32 v78, v78
	v_exp_f32_e32 v79, v79
	ds_read_b128 v[230:233], v174 offset:12288
	ds_read_b128 v[234:237], v174 offset:18432
	v_exp_f32_e32 v80, v80
	v_exp_f32_e32 v81, v81
	v_add_u32_e32 v174, s98, v207
	s_waitcnt lgkmcnt(6)
	v_mfma_f32_32x32x16_bf16 v[82:97], v[214:217], v[138:141], v[82:97]
	v_add_f32_e64 v214, v50, v66
	v_add_f32_e64 v215, v51, v67
	v_add_f32_e64 v216, v52, v68
	v_add_f32_e64 v217, v53, v69
	v_lshl_add_u32 v203, s71, 14, v115
	v_add_f32_e32 v214, v216, v214
	v_add_f32_e32 v215, v217, v215
	v_add_f32_e32 v216, v54, v70
	v_add_f32_e32 v217, v55, v71
	ds_read_b128 v[210:213], v174 offset:12288
	ds_read_b128 v[238:241], v174 offset:18432
	v_add_f32_e32 v214, v216, v214
	v_add_f32_e32 v215, v217, v215
	s_waitcnt lgkmcnt(7)
	v_mfma_f32_32x32x16_bf16 v[98:113], v[218:221], v[134:137], v[98:113]
	v_add_f32_e64 v216, v56, v72
	v_add_f32_e64 v217, v57, v73
	v_cvt_pk_bf16_f32 v50, v50, v51
	v_cvt_pk_bf16_f32 v51, v52, v53
	v_cvt_pk_bf16_f32 v52, v54, v55
	v_cvt_pk_bf16_f32 v53, v56, v57
	v_cvt_pk_bf16_f32 v54, v58, v59
	v_add_f32_e64 v214, v216, v214
	v_add_f32_e64 v215, v217, v215
	s_waitcnt lgkmcnt(6)
	v_mfma_f32_32x32x16_bf16 v[82:97], v[222:225], v[134:137], v[82:97]
	v_add_f32_e64 v216, v58, v74
	v_add_f32_e64 v217, v59, v75
	v_cvt_pk_bf16_f32 v55, v60, v61
	v_cvt_pk_bf16_f32 v56, v62, v63
	v_cvt_pk_bf16_f32 v57, v64, v65
	v_cvt_pk_bf16_f32 v58, v66, v67
	v_cvt_pk_bf16_f32 v59, v68, v69
	v_add_f32_e64 v214, v216, v214
	v_add_f32_e64 v215, v217, v215
	s_waitcnt lgkmcnt(5)
	v_mfma_f32_32x32x16_bf16 v[98:113], v[124:127], v[130:133], v[98:113]
	v_add_f32_e64 v216, v60, v76
	v_add_f32_e64 v217, v61, v77
	v_add_f32_e64 v126, v62, v78
	v_add_f32_e64 v127, v63, v79
	v_add_f32_e64 v124, v216, v214
	v_add_f32_e64 v125, v217, v215
	v_cvt_pk_bf16_f32 v60, v70, v71
	v_cvt_pk_bf16_f32 v61, v72, v73
	v_cvt_pk_bf16_f32 v62, v74, v75
	v_cvt_pk_bf16_f32 v63, v76, v77
	s_waitcnt lgkmcnt(4)
	v_mfma_f32_32x32x16_bf16 v[82:97], v[226:229], v[130:133], v[82:97]
	v_add_f32_e64 v124, v126, v124
	v_add_f32_e64 v125, v127, v125
	v_add_f32_e64 v126, v64, v80
	v_add_f32_e64 v127, v65, v81
	v_cvt_pk_bf16_f32 v64, v78, v79
	v_cvt_pk_bf16_f32 v65, v80, v81
	ds_read_b64_tr_b16 v[66:67], v203 offset:0
	ds_read_b64_tr_b16 v[68:69], v203 offset:0x400
	ds_read_b64_tr_b16 v[70:71], v203 offset:0x800
	s_waitcnt lgkmcnt(6)
	v_mfma_f32_32x32x16_bf16 v[98:113], v[230:233], v[146:149], v[98:113]
	ds_read_b64_tr_b16 v[72:73], v203 offset:0xc00
	ds_read_b64_tr_b16 v[74:75], v203 offset:0x1000
	ds_read_b64_tr_b16 v[76:77], v203 offset:0x1400
	ds_read_b64_tr_b16 v[78:79], v203 offset:0x1800
	ds_read_b64_tr_b16 v[80:81], v203 offset:0x1c00
	v_add_f32_e64 v124, v126, v124
	v_add_f32_e64 v125, v127, v125
	s_waitcnt lgkmcnt(10)
	v_mfma_f32_32x32x16_bf16 v[82:97], v[234:237], v[146:149], v[82:97]
	v_add_f32_e32 v124, v124, v125

; DEVI void finishSM(f32x16& p0, f32x16& p1, float alpha, float& l_reg, bf16x8& pa0, bf16x8& pa1, bf16x8& pa2, bf16x8& pa3) {
;     ...
;     { auto rr = __builtin_amdgcn_permlane32_swap(__float_as_uint(ps), __float_as_uint(ps), false, false);
;       ps = __uint_as_float(rr[0]) + __uint_as_float(rr[1]); }
	v_mov_b32_e32 v125, v124


; template <int OFF> DEVI s16x4 tr_read(int vb) { s16x4 r; asm volatile("ds_read_b64_tr_b16 %0, %1 offset:%2" : "=&v"(r) : "v"(vb), "i"(OFF) : "memory"); return r; }
; DEVI void pv_both(f32x16& o0, f32x16& o1, int vb, bf16x8 pa0, bf16x8 pa1, bf16x8 pa2, bf16x8 pa3) {
;     const s16x4 a0 = tr_read<v_rd_off(0, 0, 0)>(vb), b0 = tr_read<v_rd_off(0, 0, 1)>(vb), a1 = tr_read<v_rd_off(0, 1, 0)>(vb), b1 = tr_read<v_rd_off(0, 1, 1)>(vb);
;     const s16x4 a2 = tr_read<v_rd_off(0, 2, 0)>(vb), b2 = tr_read<v_rd_off(0, 2, 1)>(vb), a3 = tr_read<v_rd_off(0, 3, 0)>(vb), b3 = tr_read<v_rd_off(0, 3, 1)>(vb);
;     const s16x4 c0 = tr_read<v_rd_off(1, 0, 0)>(vb), d0 = tr_read<v_rd_off(1, 0, 1)>(vb), c1 = tr_read<v_rd_off(1, 1, 0)>(vb), d1 = tr_read<v_rd_off(1, 1, 1)>(vb);
;     const s16x4 c2 = tr_read<v_rd_off(1, 2, 0)>(vb), d2 = tr_read<v_rd_off(1, 2, 1)>(vb), c3 = tr_read<v_rd_off(1, 3, 0)>(vb), d3 = tr_read<v_rd_off(1, 3, 1)>(vb);
;     asm volatile("s_waitcnt lgkmcnt(8)" ::: "memory"); SBAR();
;     ...
;     o0 = __builtin_amdgcn_mfma_f32_32x32x16_bf16(pa0, PK(a0, b0), o0, 0, 0, 0);
;     o0 = __builtin_amdgcn_mfma_f32_32x32x16_bf16(pa1, PK(a1, b1), o0, 0, 0, 0);
;     o0 = __builtin_amdgcn_mfma_f32_32x32x16_bf16(pa2, PK(a2, b2), o0, 0, 0, 0);
;     o0 = __builtin_amdgcn_mfma_f32_32x32x16_bf16(pa3, PK(a3, b3), o0, 0, 0, 0);
;     asm volatile("s_waitcnt lgkmcnt(0)" ::: "memory"); SBAR();
;     o1 = __builtin_amdgcn_mfma_f32_32x32x16_bf16(pa0, PK(c0, d0), o1, 0, 0, 0);
;     o1 = __builtin_amdgcn_mfma_f32_32x32x16_bf16(pa1, PK(c1, d1), o1, 0, 0, 0);
;     o1 = __builtin_amdgcn_mfma_f32_32x32x16_bf16(pa2, PK(c2, d2), o1, 0, 0, 0);
;     o1 = __builtin_amdgcn_mfma_f32_32x32x16_bf16(pa3, PK(c3, d3), o1, 0, 0, 0);
;     ...
; }
; template <bool FIRST> DEVI bool partialSM(f32x16& p0, f32x16& p1, float& m_reg, float& alpha) {
;     float pmax = p0[0];
; #pragma unroll
;     for (int r = 1; r < 16; ++r) pmax = fmaxf(pmax, p0[r]);
; #pragma unroll
;     for (int r = 0; r < 16; ++r) pmax = fmaxf(pmax, p1[r]);
;     { auto rr = __builtin_amdgcn_permlane32_swap(__float_as_uint(pmax), __float_as_uint(pmax), false, false);
;       pmax = fmaxf(__uint_as_float(rr[0]), __uint_as_float(rr[1])); }
;     if (FIRST) { m_reg = pmax; alpha = 1.f;
; #pragma unroll
;         for (int r = 0; r < 16; ++r) { p0[r] = __builtin_amdgcn_exp2f(p0[r] - pmax); p1[r] = p1[r] - pmax; }
	s_waitcnt lgkmcnt(9)
	v_mfma_f32_32x32x16_bf16 v[98:113], v[210:213], v[142:145], v[98:113]
	v_permlane32_swap_b32_e32 v124, v125
	ds_read_b64_tr_b16 v[210:211], v203 offset:0x200
	ds_read_b64_tr_b16 v[212:213], v203 offset:0x600
	ds_read_b64_tr_b16 v[214:215], v203 offset:0xa00
	ds_read_b64_tr_b16 v[216:217], v203 offset:0xe00
	ds_read_b64_tr_b16 v[218:219], v203 offset:0x1200
	ds_read_b64_tr_b16 v[220:221], v203 offset:0x1600
	ds_read_b64_tr_b16 v[222:223], v203 offset:0x1a00
	s_waitcnt lgkmcnt(15)
	v_mfma_f32_32x32x16_bf16 v[82:97], v[238:241], v[142:145], v[82:97]
	ds_read_b64_tr_b16 v[224:225], v203 offset:0x1e00
	s_waitcnt lgkmcnt(14)
	v_mfma_f32_32x32x16_bf16 v[18:33], v[50:53], v[66:69], v[18:33]
	s_waitcnt lgkmcnt(6)
	v_mfma_f32_32x32x16_bf16 v[2:17], v[50:53], v[210:213], v[2:17]
	s_nop 1
	v_max_f32_e32 v249, v99, v99
	v_max_f32_e32 v250, v98, v98
	v_max_f32_e32 v249, v250, v249
	v_max3_f32 v249, v249, v100, v101
	v_max3_f32 v249, v249, v102, v103
	v_max3_f32 v251, v249, v104, v105
	v_max3_f32 v251, v251, v106, v107
	v_exp_f32_e32 v50, v98
	v_exp_f32_e32 v51, v99
	v_exp_f32_e32 v52, v100
	v_exp_f32_e32 v53, v101
	v_mfma_f32_32x32x16_bf16 v[18:33], v[54:57], v[70:73], v[18:33]
	s_waitcnt lgkmcnt(4)
	v_mfma_f32_32x32x16_bf16 v[2:17], v[54:57], v[214:217], v[2:17]
	v_max3_f32 v251, v251, v108, v109
	v_max3_f32 v251, v251, v110, v111
	v_max3_f32 v251, v251, v112, v113
	v_max3_f32 v251, v251, v82, v83
	v_max3_f32 v251, v251, v84, v85
	v_max3_f32 v251, v251, v86, v87
	v_max3_f32 v251, v251, v88, v89
	v_exp_f32_e32 v54, v102
	v_exp_f32_e32 v55, v103
	v_exp_f32_e32 v56, v104
	v_exp_f32_e32 v57, v105
	v_mfma_f32_32x32x16_bf16 v[18:33], v[58:61], v[74:77], v[18:33]
	s_waitcnt lgkmcnt(2)
	v_mfma_f32_32x32x16_bf16 v[2:17], v[58:61], v[218:221], v[2:17]
	v_max3_f32 v251, v251, v90, v91
	v_max3_f32 v251, v251, v92, v93
	v_max3_f32 v251, v251, v94, v95
	v_max3_f32 v251, v251, v96, v97
	v_mov_b32_e32 v252, v251


; template <bool FIRST> DEVI bool partialSM(f32x16& p0, f32x16& p1, float& m_reg, float& alpha) {
;     ...
;     { auto rr = __builtin_amdgcn_permlane32_swap(__float_as_uint(pmax), __float_as_uint(pmax), false, false);
;       pmax = fmaxf(__uint_as_float(rr[0]), __uint_as_float(rr[1])); }
;     if (FIRST) { m_reg = pmax; alpha = 1.f;
; #pragma unroll
;         for (int r = 0; r < 16; ++r) { p0[r] = __builtin_amdgcn_exp2f(p0[r] - pmax); p1[r] = p1[r] - pmax; }
;         return false;
;     } else if (__builtin_expect(__all(pmax <= ATT_THR), 1)) { alpha = 1.f;
; #pragma unroll
;         for (int r = 0; r < 16; ++r) p0[r] = __builtin_amdgcn_exp2f(p0[r]);
;         return false;
;     } else { const float d = fmaxf(pmax, 0.f); alpha = __builtin_amdgcn_exp2f(-d); m_reg += d;
	v_exp_f32_e32 v58, v106
	v_exp_f32_e32 v59, v107
	v_permlane32_swap_b32_e32 v251, v252
	v_exp_f32_e32 v60, v108
	v_exp_f32_e32 v61, v109
	v_mfma_f32_32x32x16_bf16 v[18:33], v[62:65], v[78:81], v[18:33]
	s_waitcnt lgkmcnt(0)
	v_mfma_f32_32x32x16_bf16 v[2:17], v[62:65], v[222:225], v[2:17]
	v_exp_f32_e32 v62, v110
	v_exp_f32_e32 v63, v111
	v_exp_f32_e32 v64, v112
	v_exp_f32_e32 v65, v113
	v_max_f32_e32 v252, v252, v252
	v_max_f32_e32 v251, v251, v251
	v_max_f32_e32 v126, v251, v252
	v_cmp_ge_f32_e32 vcc, s80, v126
	s_cmp_lg_u64 vcc, exec
	s_cselect_b64 s[6:7], -1, 0
	s_cbranch_scc1 .LBB0_2269
	v_mov_b32_e32 v209, 1.0

; DEVI void finishSM(f32x16& p0, f32x16& p1, float alpha, float& l_reg, bf16x8& pa0, bf16x8& pa1, bf16x8& pa2, bf16x8& pa3) {
; #pragma unroll
;     for (int r = 0; r < 16; ++r) p1[r] = __builtin_amdgcn_exp2f(p1[r]);
	v_exp_f32_e32 v82, v82
	v_exp_f32_e32 v83, v83
	v_exp_f32_e32 v84, v84
	v_exp_f32_e32 v85, v85
	v_exp_f32_e32 v86, v86
	v_exp_f32_e32 v87, v87
	v_exp_f32_e32 v88, v88
	v_exp_f32_e32 v89, v89
	v_exp_f32_e32 v90, v90
	v_exp_f32_e32 v91, v91
	v_exp_f32_e32 v92, v92
	v_exp_f32_e32 v93, v93
	v_exp_f32_e32 v94, v94
	v_exp_f32_e32 v95, v95
	v_exp_f32_e32 v96, v96
	v_exp_f32_e32 v97, v97
	s_branch .LBB0_2263

; DEVI void attn_unit8(const Params& p, char* smem, int unit, int l, int& cvs  , CvRun& crun) {
;     ...
;         const char* Kb = K_lds + s0 * 24576; const int vb = vb0 + s0 * 16384;
;         CvRegs cvr; cv_issue(p, l, cvs, lane, cvr, crun); cvs += (int)gridDim.x * 8;
;         qkt(pB0, pB1, Kb + 12288, qr, r32, hi, cinit);
.LBB0_2266:
	s_mul_i32 s98, s61, 0x6000
	s_add_i32 s98, s96, s98
	s_lshl_b32 s99, s61, 14
	s_add_i32 s99, s97, s99
	s_mul_i32 s6, s2, 0x6000
	s_add_i32 s6, s6, 0
	v_add_u32_e32 v249, s6, v129

; DEVI void qkt(f32x16& p0, f32x16& p1, const char* Kb, const bf16x8 (&qr)[6], int r32, int hi, const f32x16& cinit) {
; #pragma unroll
;     for (int d0 = 0; d0 < 6; ++d0) { const int cb = (d0 * 16 + hi * 8) * 2;
;         const bf16x8 k0 = *(const bf16x8*)(Kb + KSWZ(r32, cb)), k1 = *(const bf16x8*)(Kb + KSWZ(32 + r32, cb));
;         p0 = __builtin_amdgcn_mfma_f32_32x32x16_bf16(k0, qr[d0], d0 == 0 ? cinit : p0, 0, 0, 0);
;         p1 = __builtin_amdgcn_mfma_f32_32x32x16_bf16(k1, qr[d0], d0 == 0 ? cinit : p1, 0, 0, 0); }
	s_mov_b32 m0, s98
	s_barrier
	ds_read_b128 v[234:237], v249
	ds_read_b128 v[212:215], v249 offset:6144
	global_load_lds_dwordx4 v118, s[12:13]
	s_waitcnt lgkmcnt(1)
	v_mfma_f32_32x32x16_bf16 v[98:113], v[234:237], v[150:153], v[34:49]
	s_add_i32 m0, s98, 0x2000

; DEVI void qkt(f32x16& p0, f32x16& p1, const char* Kb, const bf16x8 (&qr)[6], int r32, int hi, const f32x16& cinit) {
; #pragma unroll
;     for (int d0 = 0; d0 < 6; ++d0) { const int cb = (d0 * 16 + hi * 8) * 2;
;         const bf16x8 k0 = *(const bf16x8*)(Kb + KSWZ(r32, cb)), k1 = *(const bf16x8*)(Kb + KSWZ(32 + r32, cb));
;         p0 = __builtin_amdgcn_mfma_f32_32x32x16_bf16(k0, qr[d0], d0 == 0 ? cinit : p0, 0, 0, 0);
;         p1 = __builtin_amdgcn_mfma_f32_32x32x16_bf16(k1, qr[d0], d0 == 0 ? cinit : p1, 0, 0, 0); }
	v_add_u32_e32 v126, s6, v184
	global_load_lds_dwordx4 v120, s[12:13]
	s_waitcnt lgkmcnt(0)
	v_mfma_f32_32x32x16_bf16 v[66:81], v[212:215], v[150:153], v[34:49]
	ds_read_b128 v[212:215], v126
	ds_read_b128 v[216:219], v126 offset:6144
	s_add_i32 m0, s98, 0x4000

; DEVI void qkt(f32x16& p0, f32x16& p1, const char* Kb, const bf16x8 (&qr)[6], int r32, int hi, const f32x16& cinit) {
; #pragma unroll
;     for (int d0 = 0; d0 < 6; ++d0) { const int cb = (d0 * 16 + hi * 8) * 2;
;         const bf16x8 k0 = *(const bf16x8*)(Kb + KSWZ(r32, cb)), k1 = *(const bf16x8*)(Kb + KSWZ(32 + r32, cb));
;         p0 = __builtin_amdgcn_mfma_f32_32x32x16_bf16(k0, qr[d0], d0 == 0 ? cinit : p0, 0, 0, 0);
;         p1 = __builtin_amdgcn_mfma_f32_32x32x16_bf16(k1, qr[d0], d0 == 0 ? cinit : p1, 0, 0, 0); }
	v_add_u32_e32 v126, s6, v185
	global_load_lds_dwordx4 v122, s[12:13]
	s_mov_b32 m0, s99
	s_waitcnt lgkmcnt(1)
	v_mfma_f32_32x32x16_bf16 v[98:113], v[212:215], v[138:141], v[98:113]


	global_load_lds_dwordx4 v116, s[44:45]
	s_add_i32 m0, s99, 0x2000


; template <int OFF> DEVI s16x4 tr_read(int vb) { s16x4 r; asm volatile("ds_read_b64_tr_b16 %0, %1 offset:%2" : "=&v"(r) : "v"(vb), "i"(OFF) : "memory"); return r; }
; DEVI void pv_both(f32x16& o0, f32x16& o1, int vb, bf16x8 pa0, bf16x8 pa1, bf16x8 pa2, bf16x8 pa3) {
;     const s16x4 a0 = tr_read<v_rd_off(0, 0, 0)>(vb), b0 = tr_read<v_rd_off(0, 0, 1)>(vb), a1 = tr_read<v_rd_off(0, 1, 0)>(vb), b1 = tr_read<v_rd_off(0, 1, 1)>(vb);
;     const s16x4 a2 = tr_read<v_rd_off(0, 2, 0)>(vb), b2 = tr_read<v_rd_off(0, 2, 1)>(vb), a3 = tr_read<v_rd_off(0, 3, 0)>(vb), b3 = tr_read<v_rd_off(0, 3, 1)>(vb);
;     const s16x4 c0 = tr_read<v_rd_off(1, 0, 0)>(vb), d0 = tr_read<v_rd_off(1, 0, 1)>(vb), c1 = tr_read<v_rd_off(1, 1, 0)>(vb), d1 = tr_read<v_rd_off(1, 1, 1)>(vb);
;     const s16x4 c2 = tr_read<v_rd_off(1, 2, 0)>(vb), d2 = tr_read<v_rd_off(1, 2, 1)>(vb), c3 = tr_read<v_rd_off(1, 3, 0)>(vb), d3 = tr_read<v_rd_off(1, 3, 1)>(vb);
; DEVI void finishSM(f32x16& p0, f32x16& p1, float alpha, float& l_reg, bf16x8& pa0, bf16x8& pa1, bf16x8& pa2, bf16x8& pa3) {
; #pragma unroll
;     for (int r = 0; r < 16; ++r) p1[r] = __builtin_amdgcn_exp2f(p1[r]);
;     f32x2 s2 = (f32x2){p0[0], p0[1]} + (f32x2){p1[0], p1[1]};
; #pragma unroll
;     for (int r = 2; r < 16; r += 2) s2 += (f32x2){p0[r], p0[r + 1]} + (f32x2){p1[r], p1[r + 1]};
;     float ps = s2[0] + s2[1];
;     { auto rr = __builtin_amdgcn_permlane32_swap(__float_as_uint(ps), __float_as_uint(ps), false, false);
;       ps = __uint_as_float(rr[0]) + __uint_as_float(rr[1]); }
;     l_reg = l_reg * alpha + ps;
;     ...
;     PK4(p0, 0, pa0); PK4(p0, 8, pa1); PK4(p1, 0, pa2); PK4(p1, 8, pa3);
;     ...
; }
; DEVI void qkt(f32x16& p0, f32x16& p1, const char* Kb, const bf16x8 (&qr)[6], int r32, int hi, const f32x16& cinit) {
; #pragma unroll
;     for (int d0 = 0; d0 < 6; ++d0) { const int cb = (d0 * 16 + hi * 8) * 2;
;         const bf16x8 k0 = *(const bf16x8*)(Kb + KSWZ(r32, cb)), k1 = *(const bf16x8*)(Kb + KSWZ(32 + r32, cb));
;         p0 = __builtin_amdgcn_mfma_f32_32x32x16_bf16(k0, qr[d0], d0 == 0 ? cinit : p0, 0, 0, 0);
;         p1 = __builtin_amdgcn_mfma_f32_32x32x16_bf16(k1, qr[d0], d0 == 0 ? cinit : p1, 0, 0, 0); }
	s_waitcnt lgkmcnt(0)
	v_mfma_f32_32x32x16_bf16 v[66:81], v[216:219], v[138:141], v[66:81]
	global_load_lds_dwordx4 v117, s[44:45]
	ds_read_b128 v[212:215], v126
	ds_read_b128 v[216:219], v126 offset:6144
	v_add_u32_e32 v126, s6, v205
	s_waitcnt lgkmcnt(1)
	v_mfma_f32_32x32x16_bf16 v[98:113], v[212:215], v[134:137], v[98:113]
	ds_read_b128 v[212:215], v126
	ds_read_b128 v[220:223], v126 offset:6144
	v_add_u32_e32 v126, s6, v206
	s_waitcnt lgkmcnt(2)
	v_mfma_f32_32x32x16_bf16 v[66:81], v[216:219], v[134:137], v[66:81]
	ds_read_b128 v[216:219], v126
	ds_read_b128 v[224:227], v126 offset:6144
	v_add_u32_e32 v126, s6, v207
	ds_read_b128 v[228:231], v126
	ds_read_b128 v[232:235], v126 offset:6144
	v_add_f32_e32 v126, v50, v82
	v_add_f32_e32 v127, v51, v83
	v_cvt_pk_bf16_f32 v50, v50, v51
	v_cvt_pk_bf16_f32 v51, v52, v53
	s_waitcnt lgkmcnt(5)
	v_mfma_f32_32x32x16_bf16 v[98:113], v[212:215], v[130:133], v[98:113]
	v_add_f32_e64 v212, v52, v84
	v_add_f32_e64 v213, v53, v85
	v_cvt_pk_bf16_f32 v52, v54, v55
	v_cvt_pk_bf16_f32 v53, v56, v57
	v_add_f32_e64 v126, v212, v126
	v_add_f32_e64 v127, v213, v127
	v_add_f32_e64 v212, v54, v86
	v_add_f32_e64 v213, v55, v87
	v_cvt_pk_bf16_f32 v54, v58, v59
	s_waitcnt lgkmcnt(4)
	v_mfma_f32_32x32x16_bf16 v[66:81], v[220:223], v[130:133], v[66:81]
	v_add_f32_e64 v126, v212, v126
	v_add_f32_e64 v127, v213, v127
	v_add_f32_e64 v212, v56, v88
	v_add_f32_e64 v213, v57, v89
	v_cvt_pk_bf16_f32 v55, v60, v61
	v_cvt_pk_bf16_f32 v56, v62, v63
	v_cvt_pk_bf16_f32 v57, v64, v65
	v_add_f32_e64 v126, v212, v126
	v_add_f32_e64 v127, v213, v127
	v_add_f32_e32 v212, v58, v90
	v_add_f32_e32 v213, v59, v91
	v_cvt_pk_bf16_f32 v58, v82, v83
	v_cvt_pk_bf16_f32 v59, v84, v85
	s_waitcnt lgkmcnt(3)
	v_mfma_f32_32x32x16_bf16 v[98:113], v[216:219], v[146:149], v[98:113]
	v_add_f32_e64 v126, v212, v126
	v_add_f32_e64 v127, v213, v127
	v_add_f32_e64 v212, v60, v92
	v_add_f32_e64 v213, v61, v93
	v_cvt_pk_bf16_f32 v60, v86, v87
	v_cvt_pk_bf16_f32 v61, v88, v89
	v_add_f32_e64 v126, v212, v126
	v_add_f32_e64 v127, v213, v127
	v_add_f32_e32 v212, v62, v94
	v_add_f32_e32 v213, v63, v95
	v_cvt_pk_bf16_f32 v62, v90, v91
	v_cvt_pk_bf16_f32 v63, v92, v93
	s_waitcnt lgkmcnt(2)
	v_mfma_f32_32x32x16_bf16 v[66:81], v[224:227], v[146:149], v[66:81]
	v_add_f32_e64 v126, v212, v126
	v_add_f32_e64 v127, v213, v127
	v_add_f32_e64 v212, v64, v96
	v_add_f32_e64 v213, v65, v97
	v_cvt_pk_bf16_f32 v64, v94, v95
	v_cvt_pk_bf16_f32 v65, v96, v97
	ds_read_b64_tr_b16 v[154:155], v203 offset:0x2000
	ds_read_b64_tr_b16 v[156:157], v203 offset:0x2400
	ds_read_b64_tr_b16 v[158:159], v203 offset:0x2800
	ds_read_b64_tr_b16 v[160:161], v203 offset:0x2c00
	ds_read_b64_tr_b16 v[162:163], v203 offset:0x3000
	ds_read_b64_tr_b16 v[164:165], v203 offset:0x3400
	ds_read_b64_tr_b16 v[166:167], v203 offset:0x3800
	ds_read_b64_tr_b16 v[168:169], v203 offset:0x3c00
	v_add_f32_e64 v126, v212, v126
	v_add_f32_e64 v127, v213, v127
	ds_read_b64_tr_b16 v[212:213], v203 offset:0x2200
	ds_read_b64_tr_b16 v[214:215], v203 offset:0x2600
	ds_read_b64_tr_b16 v[216:217], v203 offset:0x2a00
	s_waitcnt lgkmcnt(12)
	v_mfma_f32_32x32x16_bf16 v[98:113], v[228:231], v[142:145], v[98:113]
	ds_read_b64_tr_b16 v[218:219], v203 offset:0x2e00
	ds_read_b64_tr_b16 v[220:221], v203 offset:0x3200
	ds_read_b64_tr_b16 v[222:223], v203 offset:0x3600
	ds_read_b64_tr_b16 v[224:225], v203 offset:0x3a00
	ds_read_b64_tr_b16 v[226:227], v203 offset:0x3e00
	v_add_f32_e32 v126, v126, v127
	s_waitcnt lgkmcnt(15)
	v_mfma_f32_32x32x16_bf16 v[66:81], v[232:235], v[142:145], v[66:81]
	v_mov_b32_e32 v127, v126


; #define SBAR() __builtin_amdgcn_sched_barrier(0)
; DEVI void pv_both(f32x16& o0, f32x16& o1, int vb, bf16x8 pa0, bf16x8 pa1, bf16x8 pa2, bf16x8 pa3) {
;     ...
;     o0 = __builtin_amdgcn_mfma_f32_32x32x16_bf16(pa0, PK(a0, b0), o0, 0, 0, 0);
;     o0 = __builtin_amdgcn_mfma_f32_32x32x16_bf16(pa1, PK(a1, b1), o0, 0, 0, 0);
;     o0 = __builtin_amdgcn_mfma_f32_32x32x16_bf16(pa2, PK(a2, b2), o0, 0, 0, 0);
;     o0 = __builtin_amdgcn_mfma_f32_32x32x16_bf16(pa3, PK(a3, b3), o0, 0, 0, 0);
;     asm volatile("s_waitcnt lgkmcnt(0)" ::: "memory"); SBAR();
;     o1 = __builtin_amdgcn_mfma_f32_32x32x16_bf16(pa0, PK(c0, d0), o1, 0, 0, 0);
;     o1 = __builtin_amdgcn_mfma_f32_32x32x16_bf16(pa1, PK(c1, d1), o1, 0, 0, 0);
;     o1 = __builtin_amdgcn_mfma_f32_32x32x16_bf16(pa2, PK(c2, d2), o1, 0, 0, 0);
;     o1 = __builtin_amdgcn_mfma_f32_32x32x16_bf16(pa3, PK(c3, d3), o1, 0, 0, 0);
;     ...
; }
; template <bool FIRST> DEVI bool partialSM(f32x16& p0, f32x16& p1, float& m_reg, float& alpha) {
;     float pmax = p0[0];
; #pragma unroll
;     for (int r = 1; r < 16; ++r) pmax = fmaxf(pmax, p0[r]);
; #pragma unroll
;     for (int r = 0; r < 16; ++r) pmax = fmaxf(pmax, p1[r]);
;     { auto rr = __builtin_amdgcn_permlane32_swap(__float_as_uint(pmax), __float_as_uint(pmax), false, false);
;       pmax = fmaxf(__uint_as_float(rr[0]), __uint_as_float(rr[1])); }
;     if (FIRST) { m_reg = pmax; alpha = 1.f;
; #pragma unroll
;         for (int r = 0; r < 16; ++r) { p0[r] = __builtin_amdgcn_exp2f(p0[r] - pmax); p1[r] = p1[r] - pmax; }
;         return false;
;     } else if (__builtin_expect(__all(pmax <= ATT_THR), 1)) { alpha = 1.f;
; #pragma unroll
;         for (int r = 0; r < 16; ++r) p0[r] = __builtin_amdgcn_exp2f(p0[r]);
	s_waitcnt lgkmcnt(14)
	v_mfma_f32_32x32x16_bf16 v[18:33], v[50:53], v[154:157], v[18:33]
	v_permlane32_swap_b32_e32 v126, v127
	s_waitcnt lgkmcnt(6)
	v_mfma_f32_32x32x16_bf16 v[2:17], v[50:53], v[212:215], v[2:17]
	s_nop 1
	v_max_f32_e32 v249, v99, v99
	v_max_f32_e32 v250, v98, v98
	v_max_f32_e32 v249, v250, v249
	v_max3_f32 v249, v249, v100, v101
	v_max3_f32 v249, v249, v102, v103
	v_max3_f32 v251, v249, v104, v105
	v_max3_f32 v251, v251, v106, v107
	v_exp_f32_e32 v50, v98
	v_exp_f32_e32 v51, v99
	v_exp_f32_e32 v52, v100
	v_exp_f32_e32 v53, v101
	v_mfma_f32_32x32x16_bf16 v[18:33], v[54:57], v[158:161], v[18:33]
	s_waitcnt lgkmcnt(4)
	v_mfma_f32_32x32x16_bf16 v[2:17], v[54:57], v[216:219], v[2:17]
	v_max3_f32 v251, v251, v108, v109
	v_max3_f32 v251, v251, v110, v111
	v_max3_f32 v251, v251, v112, v113
	v_max3_f32 v251, v251, v66, v67
	v_max3_f32 v251, v251, v68, v69
	v_max3_f32 v251, v251, v70, v71
	v_max3_f32 v251, v251, v72, v73
	v_exp_f32_e32 v54, v102
	v_exp_f32_e32 v55, v103
	v_exp_f32_e32 v56, v104
	v_exp_f32_e32 v57, v105
	v_mfma_f32_32x32x16_bf16 v[18:33], v[58:61], v[162:165], v[18:33]
	s_waitcnt lgkmcnt(2)
	v_mfma_f32_32x32x16_bf16 v[2:17], v[58:61], v[220:223], v[2:17]
	v_max3_f32 v251, v251, v74, v75
	v_max3_f32 v251, v251, v76, v77
	v_max3_f32 v251, v251, v78, v79
	v_max3_f32 v251, v251, v80, v81
	v_mov_b32_e32 v252, v251


; DEVI void pv_both(f32x16& o0, f32x16& o1, int vb, bf16x8 pa0, bf16x8 pa1, bf16x8 pa2, bf16x8 pa3) {
;     ...
;     o1 = __builtin_amdgcn_mfma_f32_32x32x16_bf16(pa1, PK(c1, d1), o1, 0, 0, 0);
;     o1 = __builtin_amdgcn_mfma_f32_32x32x16_bf16(pa2, PK(c2, d2), o1, 0, 0, 0);
;     o1 = __builtin_amdgcn_mfma_f32_32x32x16_bf16(pa3, PK(c3, d3), o1, 0, 0, 0);
;     ...
; }
; template <bool FIRST> DEVI bool partialSM(f32x16& p0, f32x16& p1, float& m_reg, float& alpha) {
;     float pmax = p0[0];
; #pragma unroll
;     for (int r = 1; r < 16; ++r) pmax = fmaxf(pmax, p0[r]);
; #pragma unroll
;     for (int r = 0; r < 16; ++r) pmax = fmaxf(pmax, p1[r]);
;     { auto rr = __builtin_amdgcn_permlane32_swap(__float_as_uint(pmax), __float_as_uint(pmax), false, false);
;       pmax = fmaxf(__uint_as_float(rr[0]), __uint_as_float(rr[1])); }
;     if (FIRST) { m_reg = pmax; alpha = 1.f;
; #pragma unroll
;         for (int r = 0; r < 16; ++r) { p0[r] = __builtin_amdgcn_exp2f(p0[r] - pmax); p1[r] = p1[r] - pmax; }
;         return false;
;     } else if (__builtin_expect(__all(pmax <= ATT_THR), 1)) { alpha = 1.f;
; #pragma unroll
;         for (int r = 0; r < 16; ++r) p0[r] = __builtin_amdgcn_exp2f(p0[r]);
;         return false;
;     } else { const float d = fmaxf(pmax, 0.f); alpha = __builtin_amdgcn_exp2f(-d); m_reg += d;
	v_exp_f32_e32 v58, v106
	v_exp_f32_e32 v59, v107
	v_permlane32_swap_b32_e32 v251, v252
	v_exp_f32_e32 v60, v108
	v_exp_f32_e32 v61, v109
	v_mfma_f32_32x32x16_bf16 v[18:33], v[62:65], v[166:169], v[18:33]
	s_waitcnt lgkmcnt(0)
	v_mfma_f32_32x32x16_bf16 v[2:17], v[62:65], v[224:227], v[2:17]
	v_exp_f32_e32 v62, v110
	v_exp_f32_e32 v63, v111
	v_exp_f32_e32 v64, v112
	v_exp_f32_e32 v65, v113
	v_max_f32_e32 v252, v252, v252
	v_max_f32_e32 v251, v251, v251
	v_max_f32_e32 v174, v251, v252
	v_cmp_ge_f32_e32 vcc, s80, v174
	s_cmp_lg_u64 vcc, exec
	s_cselect_b64 s[6:7], -1, 0
	s_cbranch_scc1 .LBB0_2275
	v_mov_b32_e32 v203, 1.0

; template <bool FIRST> DEVI bool partialSM(f32x16& p0, f32x16& p1, float& m_reg, float& alpha) {
;     ...
;     } else if (__builtin_expect(__all(pmax <= ATT_THR), 1)) { alpha = 1.f;
; #pragma unroll
;         for (int r = 0; r < 16; ++r) p0[r] = __builtin_amdgcn_exp2f(p0[r]);
;         return false;
	s_branch .LBB0_2280

; #define LAS __attribute__((address_space(3)))
; DEVI int v_rd_base(int lane) { return ((lane & 3) << 3) | (((lane >> 2) & 3) << 6) | (((lane >> 4) & 1) << 5) | (((lane >> 5) & 1) << 8); }
; #define VM0() asm volatile("s_waitcnt vmcnt(0)" ::: "memory")
; template <bool FIRST> DEVI bool partialSM(f32x16& p0, f32x16& p1, float& m_reg, float& alpha) {
;     ...
;     } else { const float d = fmaxf(pmax, 0.f); alpha = __builtin_amdgcn_exp2f(-d); m_reg += d;
; #pragma unroll
;         for (int r = 0; r < 16; ++r) { p0[r] = __builtin_amdgcn_exp2f(p0[r] - d); p1[r] = p1[r] - d; }
;         return true;
; DEVI void attn_unit8(const Params& p, char* smem, int unit, int l, int& cvs  , CvRun& crun) {
;     ...
;     const int vb0 = (int)(uintptr_t)(LAS char*)V_lds + v_rd_base(lane);
;     float m_reg = 0.f, l_reg = 0.f; f32x16 o[2];
; #pragma unroll
;     for (int d = 0; d < 2; ++d)
; #pragma unroll
;         for (int r = 0; r < 16; ++r) o[d][r] = 0.f;
;     f32x16 pA0, pA1, pB0, pB1; float alA, alB; bf16x8 pa0, pa1, pa2, pa3;
;     constexpr int NTILE = S_ / 128;
;     B_DMA(0, 0); B_DMA(1, 1); VM0(); __syncthreads();
;     f32x16 cinit;
.LBB0_2269:
	v_max_f32_e32 v50, v126, v126
	v_max_f32_e32 v66, 0, v50
	v_sub_f32_e32 v50, v98, v66
	v_sub_f32_e32 v51, v99, v66
	v_sub_f32_e32 v52, v100, v66
	v_sub_f32_e32 v53, v101, v66
	v_sub_f32_e32 v54, v102, v66
	v_sub_f32_e32 v55, v103, v66
	v_sub_f32_e32 v56, v104, v66
	v_sub_f32_e32 v57, v105, v66
	v_sub_f32_e32 v58, v106, v66
	v_sub_f32_e32 v59, v107, v66
	v_sub_f32_e32 v60, v108, v66
	v_sub_f32_e32 v61, v109, v66
	v_sub_f32_e32 v62, v110, v66
	v_sub_f32_e32 v63, v111, v66
	v_sub_f32_e32 v64, v112, v66
	v_sub_f32_e32 v65, v113, v66
	v_exp_f32_e64 v209, -v66
	v_add_f32_e32 v204, v204, v66
	v_exp_f32_e32 v50, v50
	v_exp_f32_e32 v51, v51
	v_exp_f32_e32 v52, v52
	v_exp_f32_e32 v53, v53
	v_exp_f32_e32 v54, v54
	v_exp_f32_e32 v55, v55
	v_exp_f32_e32 v56, v56
	v_exp_f32_e32 v57, v57
	v_exp_f32_e32 v58, v58
	v_exp_f32_e32 v59, v59
	v_exp_f32_e32 v60, v60
	v_exp_f32_e32 v61, v61
	v_exp_f32_e32 v62, v62
	v_exp_f32_e32 v63, v63
	v_exp_f32_e32 v64, v64
	v_exp_f32_e32 v65, v65
	v_sub_f32_e32 v97, v97, v66
	v_sub_f32_e32 v96, v96, v66
	v_sub_f32_e32 v95, v95, v66
	v_sub_f32_e32 v94, v94, v66
	v_sub_f32_e32 v93, v93, v66
	v_sub_f32_e32 v92, v92, v66
	v_sub_f32_e32 v91, v91, v66
	v_sub_f32_e32 v90, v90, v66
	v_sub_f32_e32 v89, v89, v66
	v_sub_f32_e32 v88, v88, v66
	v_sub_f32_e32 v87, v87, v66
	v_sub_f32_e32 v86, v86, v66
	v_sub_f32_e32 v85, v85, v66
	v_sub_f32_e32 v84, v84, v66
	v_sub_f32_e32 v83, v83, v66
	v_sub_f32_e32 v82, v82, v66
	v_exp_f32_e32 v82, v82
	v_exp_f32_e32 v83, v83
	v_exp_f32_e32 v84, v84
	v_exp_f32_e32 v85, v85
	v_exp_f32_e32 v86, v86
	v_exp_f32_e32 v87, v87
	v_exp_f32_e32 v88, v88
	v_exp_f32_e32 v89, v89
	v_exp_f32_e32 v90, v90
	v_exp_f32_e32 v91, v91
	v_exp_f32_e32 v92, v92
	v_exp_f32_e32 v93, v93
	v_exp_f32_e32 v94, v94
	v_exp_f32_e32 v95, v95
	v_exp_f32_e32 v96, v96
	v_exp_f32_e32 v97, v97
	s_cbranch_execnz .LBB0_2262
.LBB0_2271:
	s_and_saveexec_b64 s[6:7], s[4:5]
	ds_write_b32 v188, v209 offset:128
	s_or_b64 exec, exec, s[6:7]
	v_add_u32_e32 v46, s93, v178
	s_waitcnt lgkmcnt(0)
	ds_read_b128 v[34:37], v46 offset:224
	ds_read_b128 v[38:41], v46 offset:192
	ds_read_b128 v[42:45], v46 offset:160
	ds_read_b128 v[46:49], v46 offset:128
	s_waitcnt lgkmcnt(0)
	v_pk_mul_f32 v[30:31], v[30:31], v[34:35]
	v_pk_mul_f32 v[14:15], v[14:15], v[34:35]
	v_xor_b32_e32 v34, 0x80000000, v204
	s_waitcnt lgkmcnt(2)
	v_pk_mul_f32 v[26:27], v[26:27], v[38:39]
	s_waitcnt lgkmcnt(1)
	v_pk_mul_f32 v[22:23], v[22:23], v[42:43]
	v_pk_mul_f32 v[32:33], v[32:33], v[36:37]
	v_pk_mul_f32 v[28:29], v[28:29], v[40:41]
	v_pk_mul_f32 v[24:25], v[24:25], v[44:45]
	s_waitcnt lgkmcnt(0)
	v_pk_mul_f32 v[20:21], v[20:21], v[48:49]
	v_pk_mul_f32 v[18:19], v[18:19], v[46:47]
	v_pk_mul_f32 v[10:11], v[10:11], v[38:39]
	v_pk_mul_f32 v[6:7], v[6:7], v[42:43]
	v_pk_mul_f32 v[16:17], v[16:17], v[36:37]
	v_pk_mul_f32 v[12:13], v[12:13], v[40:41]
	v_pk_mul_f32 v[8:9], v[8:9], v[44:45]
	v_pk_mul_f32 v[4:5], v[4:5], v[48:49]
	v_pk_mul_f32 v[2:3], v[2:3], v[46:47]
	v_mov_b32_e32 v35, v34
	v_mov_b32_e32 v36, v34
	v_mov_b32_e32 v37, v34
	v_mov_b32_e32 v38, v34
	v_mov_b32_e32 v39, v34
	v_mov_b32_e32 v40, v34
	v_mov_b32_e32 v41, v34
	v_mov_b32_e32 v42, v34
	v_mov_b32_e32 v43, v34
	v_mov_b32_e32 v44, v34
	v_mov_b32_e32 v45, v34
	v_mov_b32_e32 v46, v34
	v_mov_b32_e32 v47, v34
	v_mov_b32_e32 v48, v34
	v_mov_b32_e32 v49, v34
	s_andn2_b64 vcc, exec, s[14:15]
	s_mov_b64 s[6:7], -1
	s_cbranch_vccnz .LBB0_2264

; template <bool FIRST> DEVI bool partialSM(f32x16& p0, f32x16& p1, float& m_reg, float& alpha) {
;     ...
;     } else { const float d = fmaxf(pmax, 0.f); alpha = __builtin_amdgcn_exp2f(-d); m_reg += d;
; #pragma unroll
;         for (int r = 0; r < 16; ++r) { p0[r] = __builtin_amdgcn_exp2f(p0[r] - d); p1[r] = p1[r] - d; }
;         return true;
.LBB0_2275:
	v_max_f32_e32 v50, v174, v174
	v_max_f32_e32 v249, 0, v50
	v_sub_f32_e32 v50, v98, v249
	v_sub_f32_e32 v51, v99, v249
	v_sub_f32_e32 v52, v100, v249
	v_sub_f32_e32 v53, v101, v249
	v_sub_f32_e32 v54, v102, v249
	v_sub_f32_e32 v55, v103, v249
	v_sub_f32_e32 v56, v104, v249
	v_sub_f32_e32 v57, v105, v249
	v_sub_f32_e32 v58, v106, v249
	v_sub_f32_e32 v59, v107, v249
	v_sub_f32_e32 v60, v108, v249
	v_sub_f32_e32 v61, v109, v249
	v_sub_f32_e32 v62, v110, v249
	v_sub_f32_e32 v63, v111, v249
	v_sub_f32_e32 v64, v112, v249
	v_sub_f32_e32 v65, v113, v249
	v_exp_f32_e64 v203, -v249
	v_add_f32_e32 v204, v204, v249
	v_exp_f32_e32 v50, v50
	v_exp_f32_e32 v51, v51
	v_exp_f32_e32 v52, v52
	v_exp_f32_e32 v53, v53
	v_exp_f32_e32 v54, v54
	v_exp_f32_e32 v55, v55
	v_exp_f32_e32 v56, v56
	v_exp_f32_e32 v57, v57
	v_exp_f32_e32 v58, v58
	v_exp_f32_e32 v59, v59
	v_exp_f32_e32 v60, v60
	v_exp_f32_e32 v61, v61
	v_exp_f32_e32 v62, v62
	v_exp_f32_e32 v63, v63
	v_exp_f32_e32 v64, v64
	v_exp_f32_e32 v65, v65
	v_sub_f32_e32 v81, v81, v249
	v_sub_f32_e32 v80, v80, v249
	v_sub_f32_e32 v79, v79, v249
	v_sub_f32_e32 v78, v78, v249
	v_sub_f32_e32 v77, v77, v249
	v_sub_f32_e32 v76, v76, v249
	v_sub_f32_e32 v75, v75, v249
	v_sub_f32_e32 v74, v74, v249
	v_sub_f32_e32 v73, v73, v249
	v_sub_f32_e32 v72, v72, v249
	v_sub_f32_e32 v71, v71, v249
	v_sub_f32_e32 v70, v70, v249
	v_sub_f32_e32 v69, v69, v249
	v_sub_f32_e32 v68, v68, v249
	v_sub_f32_e32 v67, v67, v249
	v_sub_f32_e32 v66, v66, v249
	s_cbranch_execnz .LBB0_2268
